# P11 (layer-1 projection) epilogue: the per-row-group vmcnt(0) that only drained the previous group's stores removed (gains are waited for once in group 0)
# baseline (speedup 1.0000x reference)
; template <bool F8OUT = false> __device__ __forceinline__ void head_tile_store(const f32x4 (&acc)[2][2][4][2], bf16_t* obase  , int opitch, const float* gain, float scale, const f32x2e* rope, int row0, int fq) {
;     ...
;             const int row = row0 + ai * HALF + m * 16;
;             f32x4 x[2][2];
; #pragma unroll
;             for (int bj = 0; bj < 2; ++bj)
; #pragma unroll
;                 for (int n = 0; n < 2; ++n) x[bj][n] = acc[ai][bj][m][n];
;             if (gain) {
;                 float ss = 0.f;
; #pragma unroll
;                 for (int bj = 0; bj < 2; ++bj)
; #pragma unroll
;                     for (int n = 0; n < 2; ++n) ss += (x[bj][n][0] * x[bj][n][0] + x[bj][n][1] * x[bj][n][1]) + (x[bj][n][2] * x[bj][n][2] + x[bj][n][3] * x[bj][n][3]);
;                 ss += __shfl_xor(ss, 16); ss += __shfl_xor(ss, 32);
;                 const float r = scale / sqrtf(ss * (1.f / 64.f) + 1e-6f);
; #pragma unroll
;                 for (int bj = 0; bj < 2; ++bj)
; #pragma unroll
;                     for (int n = 0; n < 2; ++n) x[bj][n] = x[bj][n] * r * g[bj][n];
;             }
;             if (rope) {
;                 const int t = row & 8191; const bool second = (fq & 2) != 0;
; #pragma unroll
;                 for (int bj = 0; bj < 2; ++bj) { const int pos = bj ? (t & 63) : (t >> 6); const f32x2e* tb = rope + pos * 16 + 8 * (fq & 1);
; #pragma unroll
;                     for (int n = 0; n < 2; ++n)
; #pragma unroll
;                         for (int e = 0; e < 4; ++e) { const float p = __shfl_xor(x[bj][n][e], 32); const f32x2e cs = tb[4 * n + e]; const float v = x[bj][n][e];
;                             x[bj][n][e] = second ? (p * cs.y + v * cs.x) : (v * cs.x - p * cs.y); } }
;             }
;             if constexpr (F8OUT) { unsigned char* rowp8 = (unsigned char*)obase + (size_t)row * opitch + 8 * fq; typedef unsigned u32x2_ __attribute__((ext_vector_type(2)));
; #pragma unroll
;                 for (int bj = 0; bj < 2; ++bj) *(u32x2_*)(rowp8 + 32 * bj) = (u32x2_){pk4_fp8(x[bj][0][0], x[bj][0][1], x[bj][0][2], x[bj][0][3]), pk4_fp8(x[bj][1][0], x[bj][1][1], x[bj][1][2], x[bj][1][3])};
;                 continue; }
;             bf16_t* rowp = obase + (size_t)row * opitch + 8 * fq;
; #pragma unroll
.LBB0_1037:
	v_ashrrev_i32_e32 v21, 31, v20
	v_lshl_add_u64 v[22:23], v[22:23], 1, s[24:25]
	v_lshlrev_b64 v[24:25], 9, v[20:21]
	v_lshl_add_u64 v[24:25], v[22:23], 0, v[24:25]
	v_cvt_pk_bf16_f32 v182, v182, v183
	v_cvt_pk_bf16_f32 v183, v32, v33
	v_cvt_pk_bf16_f32 v184, v184, v185
	v_cvt_pk_bf16_f32 v185, v178, v179
	global_store_dwordx4 v[24:25], v[182:185], off
	v_cvt_pk_bf16_f32 v30, v30, v31
	v_cvt_pk_bf16_f32 v31, v26, v27
	v_cvt_pk_bf16_f32 v32, v180, v181
	v_cvt_pk_bf16_f32 v33, v28, v29
	global_store_dwordx4 v[24:25], v[30:33], off offset:64
	s_and_b64 vcc, exec, s[4:5]
	v_mov_b32_e32 v29, v133
	v_mov_b32_e32 v28, v132
	v_mov_b32_e32 v33, v131
	v_mov_b32_e32 v32, v130
	v_mov_b32_e32 v27, v137
	v_mov_b32_e32 v26, v136
	v_mov_b32_e32 v31, v135
	v_mov_b32_e32 v30, v134
	v_mov_b32_e32 v181, v141
	v_mov_b32_e32 v180, v140
	v_mov_b32_e32 v185, v139
	v_mov_b32_e32 v184, v138
	v_mov_b32_e32 v179, v145
	v_mov_b32_e32 v178, v144
	v_mov_b32_e32 v183, v143
	v_mov_b32_e32 v182, v142
	s_cbranch_vccnz .LBB0_1039
	v_pk_mul_f32 v[26:27], v[144:145], v[144:145]
	v_pk_mul_f32 v[28:29], v[142:143], v[142:143]
	v_mul_f32_e32 v19, v130, v130
	v_pk_mov_b32 v[30:31], v[28:29], v[26:27] op_sel:[1,0]
	v_mov_b32_e32 v29, v27
	v_pk_add_f32 v[26:27], v[30:31], v[28:29]
	v_pk_mul_f32 v[28:29], v[140:141], v[140:141]
	v_pk_mul_f32 v[30:31], v[138:139], v[138:139]
	v_pk_add_f32 v[26:27], v[26:27], v[26:27] op_sel:[0,1] op_sel_hi:[1,0]
	v_pk_mov_b32 v[32:33], v[30:31], v[28:29] op_sel:[1,0]
	v_mov_b32_e32 v31, v29
	v_pk_add_f32 v[28:29], v[32:33], v[30:31]
	v_mul_f32_e32 v30, v131, v131
	v_pk_add_f32 v[28:29], v[28:29], v[28:29] op_sel:[0,1] op_sel_hi:[1,0]
	v_mov_b32_e32 v27, v19
	v_mov_b32_e32 v29, v30
	v_pk_add_f32 v[26:27], v[26:27], v[28:29]
	v_mul_f32_e32 v28, v135, v135
	v_mul_f32_e32 v31, v132, v132
	v_pk_fma_f32 v[28:29], v[134:135], v[134:135], v[28:29] op_sel_hi:[1,1,0]
	v_mul_f32_e32 v30, v137, v137
	v_mul_f32_e32 v32, v133, v133
	v_mov_b32_e32 v29, v31
	v_pk_fma_f32 v[30:31], v[136:137], v[136:137], v[30:31] op_sel_hi:[1,1,0]
	s_nop 0
	v_mov_b32_e32 v31, v32
	v_pk_add_f32 v[28:29], v[28:29], v[30:31]
	s_nop 0
	v_pk_add_f32 v[26:27], v[26:27], v[28:29]
	s_nop 0
	v_add_f32_e32 v19, v26, v27
	v_and_b32_e32 v27, 64, v195
	v_xor_b32_e32 v26, 16, v195
	v_add_u32_e32 v27, 64, v27
	v_cmp_lt_i32_e32 vcc, v26, v27
	s_nop 1
	v_cndmask_b32_e32 v26, v195, v26, vcc
	v_lshlrev_b32_e32 v26, 2, v26
	ds_bpermute_b32 v26, v26, v19
	s_waitcnt lgkmcnt(0)
	v_add_f32_e32 v19, v19, v26
	v_xor_b32_e32 v26, 32, v195
	v_cmp_lt_i32_e32 vcc, v26, v27
	s_nop 1
	v_cndmask_b32_e32 v26, v195, v26, vcc
	v_lshlrev_b32_e32 v26, 2, v26
	ds_bpermute_b32 v26, v26, v19
	s_waitcnt lgkmcnt(0)
	v_add_f32_e32 v19, v19, v26
	v_fmamk_f32 v19, v19, 0x3c800000, v193
	v_mul_f32_e32 v26, 0x4f800000, v19
	v_cmp_gt_f32_e32 vcc, s69, v19
	s_nop 1
	v_cndmask_b32_e32 v19, v19, v26, vcc
	v_sqrt_f32_e32 v26, v19
	s_nop 0
	v_add_u32_e32 v27, -1, v26
	v_fma_f32 v28, -v27, v26, v19
	v_cmp_ge_f32_e64 s[6:7], 0, v28
	v_add_u32_e32 v28, 1, v26
	s_nop 0
	v_cndmask_b32_e64 v27, v26, v27, s[6:7]
	v_fma_f32 v26, -v28, v26, v19
	v_cmp_lt_f32_e64 s[6:7], 0, v26
	s_nop 1
	v_cndmask_b32_e64 v26, v27, v28, s[6:7]
	v_mul_f32_e32 v27, 0x37800000, v26
	v_cndmask_b32_e32 v26, v26, v27, vcc
	v_cmp_class_f32_e32 vcc, v19, v194
	s_nop 1
	v_cndmask_b32_e32 v19, v26, v19, vcc
	v_div_scale_f32 v26, s[6:7], v19, v19, 1.0
	v_rcp_f32_e32 v27, v26
	s_nop 0
	v_fma_f32 v28, -v26, v27, 1.0
	v_fmac_f32_e32 v27, v28, v27
	v_div_scale_f32 v28, vcc, 1.0, v19, 1.0
	v_mul_f32_e32 v29, v28, v27
	v_fma_f32 v30, -v26, v29, v28
	v_fmac_f32_e32 v29, v30, v27
	v_fma_f32 v26, -v26, v29, v28
	v_div_fmas_f32 v26, v26, v27, v29
	v_div_fixup_f32 v28, v26, v19, 1.0
	v_pk_mul_f32 v[26:27], v[142:143], v[28:29] op_sel_hi:[1,0]
	v_pk_mul_f32 v[30:31], v[144:145], v[28:29] op_sel_hi:[1,0]
	s_nop 0
	v_pk_mul_f32 v[182:183], v[14:15], v[26:27]
	v_pk_mul_f32 v[178:179], v[16:17], v[30:31]
	v_pk_mul_f32 v[26:27], v[138:139], v[28:29] op_sel_hi:[1,0]
	v_pk_mul_f32 v[30:31], v[140:141], v[28:29] op_sel_hi:[1,0]
	v_pk_mul_f32 v[184:185], v[6:7], v[26:27]
	v_pk_mul_f32 v[180:181], v[8:9], v[30:31]
	v_pk_mul_f32 v[30:31], v[134:135], v[28:29] op_sel_hi:[1,0]
	v_pk_mul_f32 v[26:27], v[136:137], v[28:29] op_sel_hi:[1,0]
	v_pk_mul_f32 v[32:33], v[130:131], v[28:29] op_sel_hi:[1,0]
	v_pk_mul_f32 v[28:29], v[132:133], v[28:29] op_sel_hi:[1,0]
	v_pk_mul_f32 v[26:27], v[12:13], v[26:27]
	v_pk_mul_f32 v[30:31], v[10:11], v[30:31]
	v_pk_mul_f32 v[28:29], v[4:5], v[28:29]
	v_pk_mul_f32 v[32:33], v[2:3], v[32:33]
; template <bool F8OUT = false> __device__ __forceinline__ void head_tile_store(const f32x4 (&acc)[2][2][4][2], bf16_t* obase  , int opitch, const float* gain, float scale, const f32x2e* rope, int row0, int fq) {
;     ...
;             const int row = row0 + ai * HALF + m * 16;
;             f32x4 x[2][2];
; #pragma unroll
;             for (int bj = 0; bj < 2; ++bj)
; #pragma unroll
;                 for (int n = 0; n < 2; ++n) x[bj][n] = acc[ai][bj][m][n];
;             if (gain) {
;                 float ss = 0.f;
; #pragma unroll
;                 for (int bj = 0; bj < 2; ++bj)
; #pragma unroll
;                     for (int n = 0; n < 2; ++n) ss += (x[bj][n][0] * x[bj][n][0] + x[bj][n][1] * x[bj][n][1]) + (x[bj][n][2] * x[bj][n][2] + x[bj][n][3] * x[bj][n][3]);
;                 ss += __shfl_xor(ss, 16); ss += __shfl_xor(ss, 32);
;                 const float r = scale / sqrtf(ss * (1.f / 64.f) + 1e-6f);
; #pragma unroll
;                 for (int bj = 0; bj < 2; ++bj)
; #pragma unroll
;                     for (int n = 0; n < 2; ++n) x[bj][n] = x[bj][n] * r * g[bj][n];
;             }
;             if (rope) {
;                 const int t = row & 8191; const bool second = (fq & 2) != 0;
; #pragma unroll
;                 for (int bj = 0; bj < 2; ++bj) { const int pos = bj ? (t & 63) : (t >> 6); const f32x2e* tb = rope + pos * 16 + 8 * (fq & 1);
; #pragma unroll
;                     for (int n = 0; n < 2; ++n)
; #pragma unroll
;                         for (int e = 0; e < 4; ++e) { const float p = __shfl_xor(x[bj][n][e], 32); const f32x2e cs = tb[4 * n + e]; const float v = x[bj][n][e];
;                             x[bj][n][e] = second ? (p * cs.y + v * cs.x) : (v * cs.x - p * cs.y); } }
;             }
;             if constexpr (F8OUT) { unsigned char* rowp8 = (unsigned char*)obase + (size_t)row * opitch + 8 * fq; typedef unsigned u32x2_ __attribute__((ext_vector_type(2)));
; #pragma unroll
;                 for (int bj = 0; bj < 2; ++bj) *(u32x2_*)(rowp8 + 32 * bj) = (u32x2_){pk4_fp8(x[bj][0][0], x[bj][0][1], x[bj][0][2], x[bj][0][3]), pk4_fp8(x[bj][1][0], x[bj][1][1], x[bj][1][2], x[bj][1][3])};
;                 continue; }
;             bf16_t* rowp = obase + (size_t)row * opitch + 8 * fq;
; #pragma unroll
.LBB0_1039:
	v_cvt_pk_bf16_f32 v182, v182, v183
	v_cvt_pk_bf16_f32 v183, v178, v179
	v_add_co_u32_e32 v178, vcc, 0x2000, v24
	v_lshl_add_u64 v[196:197], v[24:25], 0, s[26:27]
	s_nop 0
	v_addc_co_u32_e32 v179, vcc, 0, v25, vcc
	v_cvt_pk_bf16_f32 v184, v184, v185
	v_cvt_pk_bf16_f32 v185, v180, v181
	global_store_dwordx4 v[178:179], v[182:185], off
	v_cvt_pk_bf16_f32 v30, v30, v31
	v_cvt_pk_bf16_f32 v31, v26, v27
	v_cvt_pk_bf16_f32 v32, v32, v33
	v_cvt_pk_bf16_f32 v33, v28, v29
	global_store_dwordx4 v[196:197], v[30:33], off offset:64
	s_and_b64 vcc, exec, s[4:5]
	v_mov_b32_e32 v29, v117
	v_mov_b32_e32 v28, v116
	v_mov_b32_e32 v33, v115
	v_mov_b32_e32 v32, v114
	v_mov_b32_e32 v27, v121
	v_mov_b32_e32 v26, v120
	v_mov_b32_e32 v31, v119
	v_mov_b32_e32 v30, v118
	v_mov_b32_e32 v181, v125
	v_mov_b32_e32 v180, v124
	v_mov_b32_e32 v185, v123
	v_mov_b32_e32 v184, v122
	v_mov_b32_e32 v179, v129
	v_mov_b32_e32 v178, v128
	v_mov_b32_e32 v183, v127
	v_mov_b32_e32 v182, v126
	s_cbranch_vccnz .LBB0_1041
	v_pk_mul_f32 v[26:27], v[128:129], v[128:129]
	v_pk_mul_f32 v[28:29], v[126:127], v[126:127]
	v_mul_f32_e32 v19, v114, v114
	v_pk_mov_b32 v[30:31], v[28:29], v[26:27] op_sel:[1,0]
	v_mov_b32_e32 v29, v27
	v_pk_add_f32 v[26:27], v[30:31], v[28:29]
	v_pk_mul_f32 v[28:29], v[124:125], v[124:125]
	v_pk_mul_f32 v[30:31], v[122:123], v[122:123]
	v_pk_add_f32 v[26:27], v[26:27], v[26:27] op_sel:[0,1] op_sel_hi:[1,0]
	v_pk_mov_b32 v[32:33], v[30:31], v[28:29] op_sel:[1,0]
	v_mov_b32_e32 v31, v29
	v_pk_add_f32 v[28:29], v[32:33], v[30:31]
	v_mul_f32_e32 v30, v115, v115
	v_pk_add_f32 v[28:29], v[28:29], v[28:29] op_sel:[0,1] op_sel_hi:[1,0]
	v_mov_b32_e32 v27, v19
	v_mov_b32_e32 v29, v30
	v_pk_add_f32 v[26:27], v[26:27], v[28:29]
	v_mul_f32_e32 v28, v119, v119
	v_mul_f32_e32 v31, v116, v116
	v_pk_fma_f32 v[28:29], v[118:119], v[118:119], v[28:29] op_sel_hi:[1,1,0]
	v_mul_f32_e32 v30, v121, v121
	v_mul_f32_e32 v32, v117, v117
	v_mov_b32_e32 v29, v31
	v_pk_fma_f32 v[30:31], v[120:121], v[120:121], v[30:31] op_sel_hi:[1,1,0]
	s_nop 0
	v_mov_b32_e32 v31, v32
	v_pk_add_f32 v[28:29], v[28:29], v[30:31]
	s_nop 0
	v_pk_add_f32 v[26:27], v[26:27], v[28:29]
	s_nop 0
	v_add_f32_e32 v19, v26, v27
	v_and_b32_e32 v27, 64, v195
	v_xor_b32_e32 v26, 16, v195
	v_add_u32_e32 v27, 64, v27
	v_cmp_lt_i32_e32 vcc, v26, v27
	s_nop 1
	v_cndmask_b32_e32 v26, v195, v26, vcc
	v_lshlrev_b32_e32 v26, 2, v26
	ds_bpermute_b32 v26, v26, v19
	s_waitcnt lgkmcnt(0)
	v_add_f32_e32 v19, v19, v26
	v_xor_b32_e32 v26, 32, v195
	v_cmp_lt_i32_e32 vcc, v26, v27
	s_nop 1
	v_cndmask_b32_e32 v26, v195, v26, vcc
	v_lshlrev_b32_e32 v26, 2, v26
	ds_bpermute_b32 v26, v26, v19
	s_waitcnt lgkmcnt(0)
	v_add_f32_e32 v19, v19, v26
	v_fmamk_f32 v19, v19, 0x3c800000, v193
	v_mul_f32_e32 v26, 0x4f800000, v19
	v_cmp_gt_f32_e32 vcc, s69, v19
	s_nop 1
	v_cndmask_b32_e32 v19, v19, v26, vcc
	v_sqrt_f32_e32 v26, v19
	s_nop 0
	v_add_u32_e32 v27, -1, v26
	v_fma_f32 v28, -v27, v26, v19
	v_cmp_ge_f32_e64 s[6:7], 0, v28
	v_add_u32_e32 v28, 1, v26
	s_nop 0
	v_cndmask_b32_e64 v27, v26, v27, s[6:7]
	v_fma_f32 v26, -v28, v26, v19
	v_cmp_lt_f32_e64 s[6:7], 0, v26
	s_nop 1
	v_cndmask_b32_e64 v26, v27, v28, s[6:7]
	v_mul_f32_e32 v27, 0x37800000, v26
	v_cndmask_b32_e32 v26, v26, v27, vcc
	v_cmp_class_f32_e32 vcc, v19, v194
	s_nop 1
	v_cndmask_b32_e32 v19, v26, v19, vcc
	v_div_scale_f32 v26, s[6:7], v19, v19, 1.0
	v_rcp_f32_e32 v27, v26
	s_nop 0
	v_fma_f32 v28, -v26, v27, 1.0
	v_fmac_f32_e32 v27, v28, v27
	v_div_scale_f32 v28, vcc, 1.0, v19, 1.0
	v_mul_f32_e32 v29, v28, v27
	v_fma_f32 v30, -v26, v29, v28
	v_fmac_f32_e32 v29, v30, v27
	v_fma_f32 v26, -v26, v29, v28
	v_div_fmas_f32 v26, v26, v27, v29
	v_div_fixup_f32 v28, v26, v19, 1.0
	v_pk_mul_f32 v[26:27], v[126:127], v[28:29] op_sel_hi:[1,0]
	v_pk_mul_f32 v[30:31], v[128:129], v[28:29] op_sel_hi:[1,0]
	s_nop 0
	v_pk_mul_f32 v[182:183], v[14:15], v[26:27]
	v_pk_mul_f32 v[178:179], v[16:17], v[30:31]
	v_pk_mul_f32 v[26:27], v[122:123], v[28:29] op_sel_hi:[1,0]
	v_pk_mul_f32 v[30:31], v[124:125], v[28:29] op_sel_hi:[1,0]
	v_pk_mul_f32 v[184:185], v[6:7], v[26:27]
	v_pk_mul_f32 v[180:181], v[8:9], v[30:31]
	v_pk_mul_f32 v[30:31], v[118:119], v[28:29] op_sel_hi:[1,0]
	v_pk_mul_f32 v[26:27], v[120:121], v[28:29] op_sel_hi:[1,0]
	v_pk_mul_f32 v[32:33], v[114:115], v[28:29] op_sel_hi:[1,0]
	v_pk_mul_f32 v[28:29], v[116:117], v[28:29] op_sel_hi:[1,0]
	v_pk_mul_f32 v[26:27], v[12:13], v[26:27]
	v_pk_mul_f32 v[30:31], v[10:11], v[30:31]
	v_pk_mul_f32 v[28:29], v[4:5], v[28:29]
	v_pk_mul_f32 v[32:33], v[2:3], v[32:33]
; template <bool F8OUT = false> __device__ __forceinline__ void head_tile_store(const f32x4 (&acc)[2][2][4][2], bf16_t* obase  , int opitch, const float* gain, float scale, const f32x2e* rope, int row0, int fq) {
;     ...
;             const int row = row0 + ai * HALF + m * 16;
;             f32x4 x[2][2];
; #pragma unroll
;             for (int bj = 0; bj < 2; ++bj)
; #pragma unroll
;                 for (int n = 0; n < 2; ++n) x[bj][n] = acc[ai][bj][m][n];
;             if (gain) {
;                 float ss = 0.f;
; #pragma unroll
;                 for (int bj = 0; bj < 2; ++bj)
; #pragma unroll
;                     for (int n = 0; n < 2; ++n) ss += (x[bj][n][0] * x[bj][n][0] + x[bj][n][1] * x[bj][n][1]) + (x[bj][n][2] * x[bj][n][2] + x[bj][n][3] * x[bj][n][3]);
;                 ss += __shfl_xor(ss, 16); ss += __shfl_xor(ss, 32);
;                 const float r = scale / sqrtf(ss * (1.f / 64.f) + 1e-6f);
; #pragma unroll
;                 for (int bj = 0; bj < 2; ++bj)
; #pragma unroll
;                     for (int n = 0; n < 2; ++n) x[bj][n] = x[bj][n] * r * g[bj][n];
;             }
;             if (rope) {
;                 const int t = row & 8191; const bool second = (fq & 2) != 0;
; #pragma unroll
;                 for (int bj = 0; bj < 2; ++bj) { const int pos = bj ? (t & 63) : (t >> 6); const f32x2e* tb = rope + pos * 16 + 8 * (fq & 1);
; #pragma unroll
;                     for (int n = 0; n < 2; ++n)
; #pragma unroll
;                         for (int e = 0; e < 4; ++e) { const float p = __shfl_xor(x[bj][n][e], 32); const f32x2e cs = tb[4 * n + e]; const float v = x[bj][n][e];
;                             x[bj][n][e] = second ? (p * cs.y + v * cs.x) : (v * cs.x - p * cs.y); } }
;             }
;             if constexpr (F8OUT) { unsigned char* rowp8 = (unsigned char*)obase + (size_t)row * opitch + 8 * fq; typedef unsigned u32x2_ __attribute__((ext_vector_type(2)));
; #pragma unroll
;                 for (int bj = 0; bj < 2; ++bj) *(u32x2_*)(rowp8 + 32 * bj) = (u32x2_){pk4_fp8(x[bj][0][0], x[bj][0][1], x[bj][0][2], x[bj][0][3]), pk4_fp8(x[bj][1][0], x[bj][1][1], x[bj][1][2], x[bj][1][3])};
;                 continue; }
;             bf16_t* rowp = obase + (size_t)row * opitch + 8 * fq;
; #pragma unroll
.LBB0_1041:
	v_lshl_add_u64 v[196:197], v[24:25], 0, s[28:29]
	v_add_co_u32_e32 v24, vcc, 0x4000, v24
	v_cvt_pk_bf16_f32 v182, v182, v183
	v_cvt_pk_bf16_f32 v183, v178, v179
	v_cvt_pk_bf16_f32 v184, v184, v185
	v_cvt_pk_bf16_f32 v185, v180, v181
	s_nop 1
	v_addc_co_u32_e32 v25, vcc, 0, v25, vcc
	global_store_dwordx4 v[24:25], v[182:185], off
	v_cvt_pk_bf16_f32 v24, v30, v31
	v_cvt_pk_bf16_f32 v25, v26, v27
	v_cvt_pk_bf16_f32 v26, v32, v33
	v_cvt_pk_bf16_f32 v27, v28, v29
	global_store_dwordx4 v[196:197], v[24:27], off offset:64
	s_and_b64 vcc, exec, s[4:5]
	v_mov_b32_e32 v29, v101
	v_mov_b32_e32 v28, v100
	v_mov_b32_e32 v33, v99
	v_mov_b32_e32 v32, v98
	v_mov_b32_e32 v27, v105
	v_mov_b32_e32 v26, v104
	v_mov_b32_e32 v31, v103
	v_mov_b32_e32 v30, v102
	v_mov_b32_e32 v181, v109
	v_mov_b32_e32 v180, v108
	v_mov_b32_e32 v185, v107
	v_mov_b32_e32 v184, v106
	v_mov_b32_e32 v179, v113
	v_mov_b32_e32 v178, v112
	v_mov_b32_e32 v183, v111
	v_mov_b32_e32 v182, v110
	s_cbranch_vccnz .LBB0_1043
	v_pk_mul_f32 v[24:25], v[112:113], v[112:113]
	v_pk_mul_f32 v[26:27], v[110:111], v[110:111]
	v_mul_f32_e32 v19, v98, v98
	v_pk_mov_b32 v[28:29], v[26:27], v[24:25] op_sel:[1,0]
	v_mov_b32_e32 v27, v25
	v_pk_add_f32 v[24:25], v[28:29], v[26:27]
	v_pk_mul_f32 v[26:27], v[108:109], v[108:109]
	v_pk_mul_f32 v[28:29], v[106:107], v[106:107]
	v_pk_add_f32 v[24:25], v[24:25], v[24:25] op_sel:[0,1] op_sel_hi:[1,0]
	v_pk_mov_b32 v[30:31], v[28:29], v[26:27] op_sel:[1,0]
	v_mov_b32_e32 v29, v27
	v_pk_add_f32 v[26:27], v[30:31], v[28:29]
	v_mul_f32_e32 v28, v99, v99
	v_pk_add_f32 v[26:27], v[26:27], v[26:27] op_sel:[0,1] op_sel_hi:[1,0]
	v_mov_b32_e32 v25, v19
	v_mov_b32_e32 v27, v28
	v_pk_add_f32 v[24:25], v[24:25], v[26:27]
	v_mul_f32_e32 v26, v103, v103
	v_mul_f32_e32 v29, v100, v100
	v_pk_fma_f32 v[26:27], v[102:103], v[102:103], v[26:27] op_sel_hi:[1,1,0]
	v_mul_f32_e32 v28, v105, v105
	v_mul_f32_e32 v30, v101, v101
	v_mov_b32_e32 v27, v29
	v_pk_fma_f32 v[28:29], v[104:105], v[104:105], v[28:29] op_sel_hi:[1,1,0]
	s_nop 0
	v_mov_b32_e32 v29, v30
	v_pk_add_f32 v[26:27], v[26:27], v[28:29]
	s_nop 0
	v_pk_add_f32 v[24:25], v[24:25], v[26:27]
	s_nop 0
	v_add_f32_e32 v19, v24, v25
	v_and_b32_e32 v25, 64, v195
	v_xor_b32_e32 v24, 16, v195
	v_add_u32_e32 v25, 64, v25
	v_cmp_lt_i32_e32 vcc, v24, v25
	s_nop 1
	v_cndmask_b32_e32 v24, v195, v24, vcc
	v_lshlrev_b32_e32 v24, 2, v24
	ds_bpermute_b32 v24, v24, v19
	s_waitcnt lgkmcnt(0)
	v_add_f32_e32 v19, v19, v24
	v_xor_b32_e32 v24, 32, v195
	v_cmp_lt_i32_e32 vcc, v24, v25
	s_nop 1
	v_cndmask_b32_e32 v24, v195, v24, vcc
	v_lshlrev_b32_e32 v24, 2, v24
	ds_bpermute_b32 v24, v24, v19
	s_waitcnt lgkmcnt(0)
	v_add_f32_e32 v19, v19, v24
	v_fmamk_f32 v19, v19, 0x3c800000, v193
	v_mul_f32_e32 v24, 0x4f800000, v19
	v_cmp_gt_f32_e32 vcc, s69, v19
	s_nop 1
	v_cndmask_b32_e32 v19, v19, v24, vcc
	v_sqrt_f32_e32 v24, v19
	s_nop 0
	v_add_u32_e32 v25, -1, v24
	v_fma_f32 v26, -v25, v24, v19
	v_cmp_ge_f32_e64 s[6:7], 0, v26
	v_add_u32_e32 v26, 1, v24
	s_nop 0
	v_cndmask_b32_e64 v25, v24, v25, s[6:7]
	v_fma_f32 v24, -v26, v24, v19
	v_cmp_lt_f32_e64 s[6:7], 0, v24
	s_nop 1
	v_cndmask_b32_e64 v24, v25, v26, s[6:7]
	v_mul_f32_e32 v25, 0x37800000, v24
	v_cndmask_b32_e32 v24, v24, v25, vcc
	v_cmp_class_f32_e32 vcc, v19, v194
	s_nop 1
	v_cndmask_b32_e32 v19, v24, v19, vcc
	v_div_scale_f32 v24, s[6:7], v19, v19, 1.0
	v_rcp_f32_e32 v25, v24
	s_nop 0
	v_fma_f32 v26, -v24, v25, 1.0
	v_fmac_f32_e32 v25, v26, v25
	v_div_scale_f32 v26, vcc, 1.0, v19, 1.0
	v_mul_f32_e32 v27, v26, v25
	v_fma_f32 v28, -v24, v27, v26
	v_fmac_f32_e32 v27, v28, v25
	v_fma_f32 v24, -v24, v27, v26
	v_div_fmas_f32 v24, v24, v25, v27
	v_div_fixup_f32 v24, v24, v19, 1.0
	v_pk_mul_f32 v[26:27], v[110:111], v[24:25] op_sel_hi:[1,0]
	v_pk_mul_f32 v[28:29], v[112:113], v[24:25] op_sel_hi:[1,0]
	s_nop 0
	v_pk_mul_f32 v[182:183], v[14:15], v[26:27]
	v_pk_mul_f32 v[178:179], v[16:17], v[28:29]
	v_pk_mul_f32 v[26:27], v[106:107], v[24:25] op_sel_hi:[1,0]
	v_pk_mul_f32 v[28:29], v[108:109], v[24:25] op_sel_hi:[1,0]
	v_pk_mul_f32 v[184:185], v[6:7], v[26:27]
	v_pk_mul_f32 v[180:181], v[8:9], v[28:29]
	v_pk_mul_f32 v[28:29], v[102:103], v[24:25] op_sel_hi:[1,0]
	v_pk_mul_f32 v[26:27], v[104:105], v[24:25] op_sel_hi:[1,0]
	v_pk_mul_f32 v[32:33], v[98:99], v[24:25] op_sel_hi:[1,0]
	v_pk_mul_f32 v[24:25], v[100:101], v[24:25] op_sel_hi:[1,0]
	v_pk_mul_f32 v[26:27], v[12:13], v[26:27]
	v_pk_mul_f32 v[30:31], v[10:11], v[28:29]
	v_pk_mul_f32 v[28:29], v[4:5], v[24:25]
	v_pk_mul_f32 v[32:33], v[2:3], v[32:33]
; template <bool F8OUT = false> __device__ __forceinline__ void head_tile_store(const f32x4 (&acc)[2][2][4][2], bf16_t* obase  , int opitch, const float* gain, float scale, const f32x2e* rope, int row0, int fq) {
;     ...
;             const int row = row0 + ai * HALF + m * 16;
;             f32x4 x[2][2];
; #pragma unroll
;             for (int bj = 0; bj < 2; ++bj)
; #pragma unroll
;                 for (int n = 0; n < 2; ++n) x[bj][n] = acc[ai][bj][m][n];
;             if (gain) {
;                 float ss = 0.f;
; #pragma unroll
;                 for (int bj = 0; bj < 2; ++bj)
; #pragma unroll
;                     for (int n = 0; n < 2; ++n) ss += (x[bj][n][0] * x[bj][n][0] + x[bj][n][1] * x[bj][n][1]) + (x[bj][n][2] * x[bj][n][2] + x[bj][n][3] * x[bj][n][3]);
;                 ss += __shfl_xor(ss, 16); ss += __shfl_xor(ss, 32);
;                 const float r = scale / sqrtf(ss * (1.f / 64.f) + 1e-6f);
; #pragma unroll
;                 for (int bj = 0; bj < 2; ++bj)
; #pragma unroll
;                     for (int n = 0; n < 2; ++n) x[bj][n] = x[bj][n] * r * g[bj][n];
;             }
;             if (rope) {
;                 const int t = row & 8191; const bool second = (fq & 2) != 0;
; #pragma unroll
;                 for (int bj = 0; bj < 2; ++bj) { const int pos = bj ? (t & 63) : (t >> 6); const f32x2e* tb = rope + pos * 16 + 8 * (fq & 1);
; #pragma unroll
;                     for (int n = 0; n < 2; ++n)
; #pragma unroll
;                         for (int e = 0; e < 4; ++e) { const float p = __shfl_xor(x[bj][n][e], 32); const f32x2e cs = tb[4 * n + e]; const float v = x[bj][n][e];
;                             x[bj][n][e] = second ? (p * cs.y + v * cs.x) : (v * cs.x - p * cs.y); } }
;             }
;             if constexpr (F8OUT) { unsigned char* rowp8 = (unsigned char*)obase + (size_t)row * opitch + 8 * fq; typedef unsigned u32x2_ __attribute__((ext_vector_type(2)));
; #pragma unroll
;                 for (int bj = 0; bj < 2; ++bj) *(u32x2_*)(rowp8 + 32 * bj) = (u32x2_){pk4_fp8(x[bj][0][0], x[bj][0][1], x[bj][0][2], x[bj][0][3]), pk4_fp8(x[bj][1][0], x[bj][1][1], x[bj][1][2], x[bj][1][3])};
;                 continue; }
;             bf16_t* rowp = obase + (size_t)row * opitch + 8 * fq;
; #pragma unroll
.LBB0_1043:
	v_lshlrev_b64 v[24:25], 9, v[20:21]
	v_lshl_add_u64 v[24:25], v[22:23], 0, v[24:25]
	v_cvt_pk_bf16_f32 v182, v182, v183
	v_cvt_pk_bf16_f32 v183, v178, v179
	v_add_co_u32_e32 v178, vcc, 0x6000, v24
	v_lshl_add_u64 v[196:197], v[24:25], 0, s[30:31]
	s_nop 0
	v_addc_co_u32_e32 v179, vcc, 0, v25, vcc
	v_cvt_pk_bf16_f32 v184, v184, v185
	v_cvt_pk_bf16_f32 v185, v180, v181
	global_store_dwordx4 v[178:179], v[182:185], off
	v_cvt_pk_bf16_f32 v30, v30, v31
	v_cvt_pk_bf16_f32 v31, v26, v27
	v_cvt_pk_bf16_f32 v32, v32, v33
	v_cvt_pk_bf16_f32 v33, v28, v29
	global_store_dwordx4 v[196:197], v[30:33], off offset:64
	s_and_b64 vcc, exec, s[4:5]
	v_mov_b32_e32 v29, v85
	v_mov_b32_e32 v28, v84
	v_mov_b32_e32 v33, v83
	v_mov_b32_e32 v32, v82
	v_mov_b32_e32 v27, v89
	v_mov_b32_e32 v26, v88
	v_mov_b32_e32 v31, v87
	v_mov_b32_e32 v30, v86
	v_mov_b32_e32 v181, v93
	v_mov_b32_e32 v180, v92
	v_mov_b32_e32 v185, v91
	v_mov_b32_e32 v184, v90
	v_mov_b32_e32 v179, v97
	v_mov_b32_e32 v178, v96
	v_mov_b32_e32 v183, v95
	v_mov_b32_e32 v182, v94
	s_cbranch_vccnz .LBB0_1045
	v_pk_mul_f32 v[26:27], v[96:97], v[96:97]
	v_pk_mul_f32 v[28:29], v[94:95], v[94:95]
	v_mul_f32_e32 v19, v82, v82
	v_pk_mov_b32 v[30:31], v[28:29], v[26:27] op_sel:[1,0]
	v_mov_b32_e32 v29, v27
	v_pk_add_f32 v[26:27], v[30:31], v[28:29]
	v_pk_mul_f32 v[28:29], v[92:93], v[92:93]
	v_pk_mul_f32 v[30:31], v[90:91], v[90:91]
	v_pk_add_f32 v[26:27], v[26:27], v[26:27] op_sel:[0,1] op_sel_hi:[1,0]
	v_pk_mov_b32 v[32:33], v[30:31], v[28:29] op_sel:[1,0]
	v_mov_b32_e32 v31, v29
	v_pk_add_f32 v[28:29], v[32:33], v[30:31]
	v_mul_f32_e32 v30, v83, v83
	v_pk_add_f32 v[28:29], v[28:29], v[28:29] op_sel:[0,1] op_sel_hi:[1,0]
	v_mov_b32_e32 v27, v19
	v_mov_b32_e32 v29, v30
	v_pk_add_f32 v[26:27], v[26:27], v[28:29]
	v_mul_f32_e32 v28, v87, v87
	v_mul_f32_e32 v31, v84, v84
	v_pk_fma_f32 v[28:29], v[86:87], v[86:87], v[28:29] op_sel_hi:[1,1,0]
	v_mul_f32_e32 v30, v89, v89
	v_mul_f32_e32 v32, v85, v85
	v_mov_b32_e32 v29, v31
	v_pk_fma_f32 v[30:31], v[88:89], v[88:89], v[30:31] op_sel_hi:[1,1,0]
	s_nop 0
	v_mov_b32_e32 v31, v32
	v_pk_add_f32 v[28:29], v[28:29], v[30:31]
	s_nop 0
	v_pk_add_f32 v[26:27], v[26:27], v[28:29]
	s_nop 0
	v_add_f32_e32 v19, v26, v27
	v_and_b32_e32 v27, 64, v195
	v_xor_b32_e32 v26, 16, v195
	v_add_u32_e32 v27, 64, v27
	v_cmp_lt_i32_e32 vcc, v26, v27
	s_nop 1
	v_cndmask_b32_e32 v26, v195, v26, vcc
	v_lshlrev_b32_e32 v26, 2, v26
	ds_bpermute_b32 v26, v26, v19
	s_waitcnt lgkmcnt(0)
	v_add_f32_e32 v19, v19, v26
	v_xor_b32_e32 v26, 32, v195
	v_cmp_lt_i32_e32 vcc, v26, v27
	s_nop 1
	v_cndmask_b32_e32 v26, v195, v26, vcc
	v_lshlrev_b32_e32 v26, 2, v26
	ds_bpermute_b32 v26, v26, v19
	s_waitcnt lgkmcnt(0)
	v_add_f32_e32 v19, v19, v26
	v_fmamk_f32 v19, v19, 0x3c800000, v193
	v_mul_f32_e32 v26, 0x4f800000, v19
	v_cmp_gt_f32_e32 vcc, s69, v19
	s_nop 1
	v_cndmask_b32_e32 v19, v19, v26, vcc
	v_sqrt_f32_e32 v26, v19
	s_nop 0
	v_add_u32_e32 v27, -1, v26
	v_fma_f32 v28, -v27, v26, v19
	v_cmp_ge_f32_e64 s[6:7], 0, v28
	v_add_u32_e32 v28, 1, v26
	s_nop 0
	v_cndmask_b32_e64 v27, v26, v27, s[6:7]
	v_fma_f32 v26, -v28, v26, v19
	v_cmp_lt_f32_e64 s[6:7], 0, v26
	s_nop 1
	v_cndmask_b32_e64 v26, v27, v28, s[6:7]
	v_mul_f32_e32 v27, 0x37800000, v26
	v_cndmask_b32_e32 v26, v26, v27, vcc
	v_cmp_class_f32_e32 vcc, v19, v194
	s_nop 1
	v_cndmask_b32_e32 v19, v26, v19, vcc
	v_div_scale_f32 v26, s[6:7], v19, v19, 1.0
	v_rcp_f32_e32 v27, v26
	s_nop 0
	v_fma_f32 v28, -v26, v27, 1.0
	v_fmac_f32_e32 v27, v28, v27
	v_div_scale_f32 v28, vcc, 1.0, v19, 1.0
	v_mul_f32_e32 v29, v28, v27
	v_fma_f32 v30, -v26, v29, v28
	v_fmac_f32_e32 v29, v30, v27
	v_fma_f32 v26, -v26, v29, v28
	v_div_fmas_f32 v26, v26, v27, v29
	v_div_fixup_f32 v28, v26, v19, 1.0
	v_pk_mul_f32 v[26:27], v[94:95], v[28:29] op_sel_hi:[1,0]
	v_pk_mul_f32 v[30:31], v[96:97], v[28:29] op_sel_hi:[1,0]
	s_nop 0
	v_pk_mul_f32 v[182:183], v[14:15], v[26:27]
	v_pk_mul_f32 v[178:179], v[16:17], v[30:31]
	v_pk_mul_f32 v[26:27], v[90:91], v[28:29] op_sel_hi:[1,0]
	v_pk_mul_f32 v[30:31], v[92:93], v[28:29] op_sel_hi:[1,0]
	v_pk_mul_f32 v[184:185], v[6:7], v[26:27]
	v_pk_mul_f32 v[180:181], v[8:9], v[30:31]
	v_pk_mul_f32 v[30:31], v[86:87], v[28:29] op_sel_hi:[1,0]
	v_pk_mul_f32 v[26:27], v[88:89], v[28:29] op_sel_hi:[1,0]
	v_pk_mul_f32 v[32:33], v[82:83], v[28:29] op_sel_hi:[1,0]
	v_pk_mul_f32 v[28:29], v[84:85], v[28:29] op_sel_hi:[1,0]
	v_pk_mul_f32 v[26:27], v[12:13], v[26:27]
	v_pk_mul_f32 v[30:31], v[10:11], v[30:31]
	v_pk_mul_f32 v[28:29], v[4:5], v[28:29]
	v_pk_mul_f32 v[32:33], v[2:3], v[32:33]
; template <bool F8OUT = false> __device__ __forceinline__ void head_tile_store(const f32x4 (&acc)[2][2][4][2], bf16_t* obase  , int opitch, const float* gain, float scale, const f32x2e* rope, int row0, int fq) {
;     ...
;             const int row = row0 + ai * HALF + m * 16;
;             f32x4 x[2][2];
; #pragma unroll
;             for (int bj = 0; bj < 2; ++bj)
; #pragma unroll
;                 for (int n = 0; n < 2; ++n) x[bj][n] = acc[ai][bj][m][n];
;             if (gain) {
;                 float ss = 0.f;
; #pragma unroll
;                 for (int bj = 0; bj < 2; ++bj)
; #pragma unroll
;                     for (int n = 0; n < 2; ++n) ss += (x[bj][n][0] * x[bj][n][0] + x[bj][n][1] * x[bj][n][1]) + (x[bj][n][2] * x[bj][n][2] + x[bj][n][3] * x[bj][n][3]);
;                 ss += __shfl_xor(ss, 16); ss += __shfl_xor(ss, 32);
;                 const float r = scale / sqrtf(ss * (1.f / 64.f) + 1e-6f);
; #pragma unroll
;                 for (int bj = 0; bj < 2; ++bj)
; #pragma unroll
;                     for (int n = 0; n < 2; ++n) x[bj][n] = x[bj][n] * r * g[bj][n];
;             }
;             if (rope) {
;                 const int t = row & 8191; const bool second = (fq & 2) != 0;
; #pragma unroll
;                 for (int bj = 0; bj < 2; ++bj) { const int pos = bj ? (t & 63) : (t >> 6); const f32x2e* tb = rope + pos * 16 + 8 * (fq & 1);
; #pragma unroll
;                     for (int n = 0; n < 2; ++n)
; #pragma unroll
;                         for (int e = 0; e < 4; ++e) { const float p = __shfl_xor(x[bj][n][e], 32); const f32x2e cs = tb[4 * n + e]; const float v = x[bj][n][e];
;                             x[bj][n][e] = second ? (p * cs.y + v * cs.x) : (v * cs.x - p * cs.y); } }
;             }
;             if constexpr (F8OUT) { unsigned char* rowp8 = (unsigned char*)obase + (size_t)row * opitch + 8 * fq; typedef unsigned u32x2_ __attribute__((ext_vector_type(2)));
; #pragma unroll
;                 for (int bj = 0; bj < 2; ++bj) *(u32x2_*)(rowp8 + 32 * bj) = (u32x2_){pk4_fp8(x[bj][0][0], x[bj][0][1], x[bj][0][2], x[bj][0][3]), pk4_fp8(x[bj][1][0], x[bj][1][1], x[bj][1][2], x[bj][1][3])};
;                 continue; }
;             bf16_t* rowp = obase + (size_t)row * opitch + 8 * fq;
; #pragma unroll
.LBB0_1045:
	v_lshl_add_u64 v[196:197], v[24:25], 0, s[34:35]
	v_add_co_u32_e32 v24, vcc, 0x10000, v24
	v_cvt_pk_bf16_f32 v182, v182, v183
	v_cvt_pk_bf16_f32 v183, v178, v179
	v_cvt_pk_bf16_f32 v184, v184, v185
	v_cvt_pk_bf16_f32 v185, v180, v181
	s_nop 1
	v_addc_co_u32_e32 v25, vcc, 0, v25, vcc
	global_store_dwordx4 v[24:25], v[182:185], off
	v_cvt_pk_bf16_f32 v24, v30, v31
	v_cvt_pk_bf16_f32 v25, v26, v27
	v_cvt_pk_bf16_f32 v26, v32, v33
	v_cvt_pk_bf16_f32 v27, v28, v29
	global_store_dwordx4 v[196:197], v[24:27], off offset:64
	s_and_b64 vcc, exec, s[4:5]
	v_mov_b32_e32 v29, v69
	v_mov_b32_e32 v28, v68
	v_mov_b32_e32 v33, v67
	v_mov_b32_e32 v32, v66
	v_mov_b32_e32 v27, v73
	v_mov_b32_e32 v26, v72
	v_mov_b32_e32 v31, v71
	v_mov_b32_e32 v30, v70
	v_mov_b32_e32 v181, v77
	v_mov_b32_e32 v180, v76
	v_mov_b32_e32 v185, v75
	v_mov_b32_e32 v184, v74
	v_mov_b32_e32 v179, v81
	v_mov_b32_e32 v178, v80
	v_mov_b32_e32 v183, v79
	v_mov_b32_e32 v182, v78
	s_cbranch_vccnz .LBB0_1047
	v_pk_mul_f32 v[24:25], v[80:81], v[80:81]
	v_pk_mul_f32 v[26:27], v[78:79], v[78:79]
	v_mul_f32_e32 v19, v66, v66
	v_pk_mov_b32 v[28:29], v[26:27], v[24:25] op_sel:[1,0]
	v_mov_b32_e32 v27, v25
	v_pk_add_f32 v[24:25], v[28:29], v[26:27]
	v_pk_mul_f32 v[26:27], v[76:77], v[76:77]
	v_pk_mul_f32 v[28:29], v[74:75], v[74:75]
	v_pk_add_f32 v[24:25], v[24:25], v[24:25] op_sel:[0,1] op_sel_hi:[1,0]
	v_pk_mov_b32 v[30:31], v[28:29], v[26:27] op_sel:[1,0]
	v_mov_b32_e32 v29, v27
	v_pk_add_f32 v[26:27], v[30:31], v[28:29]
	v_mul_f32_e32 v28, v67, v67
	v_pk_add_f32 v[26:27], v[26:27], v[26:27] op_sel:[0,1] op_sel_hi:[1,0]
	v_mov_b32_e32 v25, v19
	v_mov_b32_e32 v27, v28
	v_pk_add_f32 v[24:25], v[24:25], v[26:27]
	v_mul_f32_e32 v26, v71, v71
	v_mul_f32_e32 v29, v68, v68
	v_pk_fma_f32 v[26:27], v[70:71], v[70:71], v[26:27] op_sel_hi:[1,1,0]
	v_mul_f32_e32 v28, v73, v73
	v_mul_f32_e32 v30, v69, v69
	v_mov_b32_e32 v27, v29
	v_pk_fma_f32 v[28:29], v[72:73], v[72:73], v[28:29] op_sel_hi:[1,1,0]
	s_nop 0
	v_mov_b32_e32 v29, v30
	v_pk_add_f32 v[26:27], v[26:27], v[28:29]
	s_nop 0
	v_pk_add_f32 v[24:25], v[24:25], v[26:27]
	s_nop 0
	v_add_f32_e32 v19, v24, v25
	v_and_b32_e32 v25, 64, v195
	v_xor_b32_e32 v24, 16, v195
	v_add_u32_e32 v25, 64, v25
	v_cmp_lt_i32_e32 vcc, v24, v25
	s_nop 1
	v_cndmask_b32_e32 v24, v195, v24, vcc
	v_lshlrev_b32_e32 v24, 2, v24
	ds_bpermute_b32 v24, v24, v19
	s_waitcnt lgkmcnt(0)
	v_add_f32_e32 v19, v19, v24
	v_xor_b32_e32 v24, 32, v195
	v_cmp_lt_i32_e32 vcc, v24, v25
	s_nop 1
	v_cndmask_b32_e32 v24, v195, v24, vcc
	v_lshlrev_b32_e32 v24, 2, v24
	ds_bpermute_b32 v24, v24, v19
	s_waitcnt lgkmcnt(0)
	v_add_f32_e32 v19, v19, v24
	v_fmamk_f32 v19, v19, 0x3c800000, v193
	v_mul_f32_e32 v24, 0x4f800000, v19
	v_cmp_gt_f32_e32 vcc, s69, v19
	s_nop 1
	v_cndmask_b32_e32 v19, v19, v24, vcc
	v_sqrt_f32_e32 v24, v19
	s_nop 0
	v_add_u32_e32 v25, -1, v24
	v_fma_f32 v26, -v25, v24, v19
	v_cmp_ge_f32_e64 s[6:7], 0, v26
	v_add_u32_e32 v26, 1, v24
	s_nop 0
	v_cndmask_b32_e64 v25, v24, v25, s[6:7]
	v_fma_f32 v24, -v26, v24, v19
	v_cmp_lt_f32_e64 s[6:7], 0, v24
	s_nop 1
	v_cndmask_b32_e64 v24, v25, v26, s[6:7]
	v_mul_f32_e32 v25, 0x37800000, v24
	v_cndmask_b32_e32 v24, v24, v25, vcc
	v_cmp_class_f32_e32 vcc, v19, v194
	s_nop 1
	v_cndmask_b32_e32 v19, v24, v19, vcc
	v_div_scale_f32 v24, s[6:7], v19, v19, 1.0
	v_rcp_f32_e32 v25, v24
	s_nop 0
	v_fma_f32 v26, -v24, v25, 1.0
	v_fmac_f32_e32 v25, v26, v25
	v_div_scale_f32 v26, vcc, 1.0, v19, 1.0
	v_mul_f32_e32 v27, v26, v25
	v_fma_f32 v28, -v24, v27, v26
	v_fmac_f32_e32 v27, v28, v25
	v_fma_f32 v24, -v24, v27, v26
	v_div_fmas_f32 v24, v24, v25, v27
	v_div_fixup_f32 v24, v24, v19, 1.0
	v_pk_mul_f32 v[26:27], v[78:79], v[24:25] op_sel_hi:[1,0]
	v_pk_mul_f32 v[28:29], v[80:81], v[24:25] op_sel_hi:[1,0]
	s_nop 0
	v_pk_mul_f32 v[182:183], v[14:15], v[26:27]
	v_pk_mul_f32 v[178:179], v[16:17], v[28:29]
	v_pk_mul_f32 v[26:27], v[74:75], v[24:25] op_sel_hi:[1,0]
	v_pk_mul_f32 v[28:29], v[76:77], v[24:25] op_sel_hi:[1,0]
	v_pk_mul_f32 v[184:185], v[6:7], v[26:27]
	v_pk_mul_f32 v[180:181], v[8:9], v[28:29]
	v_pk_mul_f32 v[28:29], v[70:71], v[24:25] op_sel_hi:[1,0]
	v_pk_mul_f32 v[26:27], v[72:73], v[24:25] op_sel_hi:[1,0]
	v_pk_mul_f32 v[32:33], v[66:67], v[24:25] op_sel_hi:[1,0]
	v_pk_mul_f32 v[24:25], v[68:69], v[24:25] op_sel_hi:[1,0]
	v_pk_mul_f32 v[26:27], v[12:13], v[26:27]
	v_pk_mul_f32 v[30:31], v[10:11], v[28:29]
	v_pk_mul_f32 v[28:29], v[4:5], v[24:25]
	v_pk_mul_f32 v[32:33], v[2:3], v[32:33]
; template <bool F8OUT = false> __device__ __forceinline__ void head_tile_store(const f32x4 (&acc)[2][2][4][2], bf16_t* obase  , int opitch, const float* gain, float scale, const f32x2e* rope, int row0, int fq) {
;     ...
;             const int row = row0 + ai * HALF + m * 16;
;             f32x4 x[2][2];
; #pragma unroll
;             for (int bj = 0; bj < 2; ++bj)
; #pragma unroll
;                 for (int n = 0; n < 2; ++n) x[bj][n] = acc[ai][bj][m][n];
;             if (gain) {
;                 float ss = 0.f;
; #pragma unroll
;                 for (int bj = 0; bj < 2; ++bj)
; #pragma unroll
;                     for (int n = 0; n < 2; ++n) ss += (x[bj][n][0] * x[bj][n][0] + x[bj][n][1] * x[bj][n][1]) + (x[bj][n][2] * x[bj][n][2] + x[bj][n][3] * x[bj][n][3]);
;                 ss += __shfl_xor(ss, 16); ss += __shfl_xor(ss, 32);
;                 const float r = scale / sqrtf(ss * (1.f / 64.f) + 1e-6f);
; #pragma unroll
;                 for (int bj = 0; bj < 2; ++bj)
; #pragma unroll
;                     for (int n = 0; n < 2; ++n) x[bj][n] = x[bj][n] * r * g[bj][n];
;             }
;             if (rope) {
;                 const int t = row & 8191; const bool second = (fq & 2) != 0;
; #pragma unroll
;                 for (int bj = 0; bj < 2; ++bj) { const int pos = bj ? (t & 63) : (t >> 6); const f32x2e* tb = rope + pos * 16 + 8 * (fq & 1);
; #pragma unroll
;                     for (int n = 0; n < 2; ++n)
; #pragma unroll
;                         for (int e = 0; e < 4; ++e) { const float p = __shfl_xor(x[bj][n][e], 32); const f32x2e cs = tb[4 * n + e]; const float v = x[bj][n][e];
;                             x[bj][n][e] = second ? (p * cs.y + v * cs.x) : (v * cs.x - p * cs.y); } }
;             }
;             if constexpr (F8OUT) { unsigned char* rowp8 = (unsigned char*)obase + (size_t)row * opitch + 8 * fq; typedef unsigned u32x2_ __attribute__((ext_vector_type(2)));
; #pragma unroll
;                 for (int bj = 0; bj < 2; ++bj) *(u32x2_*)(rowp8 + 32 * bj) = (u32x2_){pk4_fp8(x[bj][0][0], x[bj][0][1], x[bj][0][2], x[bj][0][3]), pk4_fp8(x[bj][1][0], x[bj][1][1], x[bj][1][2], x[bj][1][3])};
;                 continue; }
;             bf16_t* rowp = obase + (size_t)row * opitch + 8 * fq;
; #pragma unroll
.LBB0_1047:
	v_lshlrev_b64 v[24:25], 9, v[20:21]
	v_lshl_add_u64 v[24:25], v[22:23], 0, v[24:25]
	v_cvt_pk_bf16_f32 v182, v182, v183
	v_cvt_pk_bf16_f32 v183, v178, v179
	v_add_co_u32_e32 v178, vcc, 0x12000, v24
	v_lshl_add_u64 v[196:197], v[24:25], 0, s[36:37]
	s_nop 0
	v_addc_co_u32_e32 v179, vcc, 0, v25, vcc
	v_cvt_pk_bf16_f32 v184, v184, v185
	v_cvt_pk_bf16_f32 v185, v180, v181
	global_store_dwordx4 v[178:179], v[182:185], off
	v_cvt_pk_bf16_f32 v30, v30, v31
	v_cvt_pk_bf16_f32 v31, v26, v27
	v_cvt_pk_bf16_f32 v32, v32, v33
	v_cvt_pk_bf16_f32 v33, v28, v29
	global_store_dwordx4 v[196:197], v[30:33], off offset:64
	s_and_b64 vcc, exec, s[4:5]
	v_mov_b32_e32 v29, v53
	v_mov_b32_e32 v28, v52
	v_mov_b32_e32 v33, v51
	v_mov_b32_e32 v32, v50
	v_mov_b32_e32 v27, v57
	v_mov_b32_e32 v26, v56
	v_mov_b32_e32 v31, v55
	v_mov_b32_e32 v30, v54
	v_mov_b32_e32 v181, v61
	v_mov_b32_e32 v180, v60
	v_mov_b32_e32 v185, v59
	v_mov_b32_e32 v184, v58
	v_mov_b32_e32 v179, v65
	v_mov_b32_e32 v178, v64
	v_mov_b32_e32 v183, v63
	v_mov_b32_e32 v182, v62
	s_cbranch_vccnz .LBB0_1049
	v_pk_mul_f32 v[26:27], v[64:65], v[64:65]
	v_pk_mul_f32 v[28:29], v[62:63], v[62:63]
	v_mul_f32_e32 v19, v50, v50
	v_pk_mov_b32 v[30:31], v[28:29], v[26:27] op_sel:[1,0]
	v_mov_b32_e32 v29, v27
	v_pk_add_f32 v[26:27], v[30:31], v[28:29]
	v_pk_mul_f32 v[28:29], v[60:61], v[60:61]
	v_pk_mul_f32 v[30:31], v[58:59], v[58:59]
	v_pk_add_f32 v[26:27], v[26:27], v[26:27] op_sel:[0,1] op_sel_hi:[1,0]
	v_pk_mov_b32 v[32:33], v[30:31], v[28:29] op_sel:[1,0]
	v_mov_b32_e32 v31, v29
	v_pk_add_f32 v[28:29], v[32:33], v[30:31]
	v_mul_f32_e32 v30, v51, v51
	v_pk_add_f32 v[28:29], v[28:29], v[28:29] op_sel:[0,1] op_sel_hi:[1,0]
	v_mov_b32_e32 v27, v19
	v_mov_b32_e32 v29, v30
	v_pk_add_f32 v[26:27], v[26:27], v[28:29]
	v_mul_f32_e32 v28, v55, v55
	v_mul_f32_e32 v31, v52, v52
	v_pk_fma_f32 v[28:29], v[54:55], v[54:55], v[28:29] op_sel_hi:[1,1,0]
	v_mul_f32_e32 v30, v57, v57
	v_mul_f32_e32 v32, v53, v53
	v_mov_b32_e32 v29, v31
	v_pk_fma_f32 v[30:31], v[56:57], v[56:57], v[30:31] op_sel_hi:[1,1,0]
	s_nop 0
	v_mov_b32_e32 v31, v32
	v_pk_add_f32 v[28:29], v[28:29], v[30:31]
	s_nop 0
	v_pk_add_f32 v[26:27], v[26:27], v[28:29]
	s_nop 0
	v_add_f32_e32 v19, v26, v27
	v_and_b32_e32 v27, 64, v195
	v_xor_b32_e32 v26, 16, v195
	v_add_u32_e32 v27, 64, v27
	v_cmp_lt_i32_e32 vcc, v26, v27
	s_nop 1
	v_cndmask_b32_e32 v26, v195, v26, vcc
	v_lshlrev_b32_e32 v26, 2, v26
	ds_bpermute_b32 v26, v26, v19
	s_waitcnt lgkmcnt(0)
	v_add_f32_e32 v19, v19, v26
	v_xor_b32_e32 v26, 32, v195
	v_cmp_lt_i32_e32 vcc, v26, v27
	s_nop 1
	v_cndmask_b32_e32 v26, v195, v26, vcc
	v_lshlrev_b32_e32 v26, 2, v26
	ds_bpermute_b32 v26, v26, v19
	s_waitcnt lgkmcnt(0)
	v_add_f32_e32 v19, v19, v26
	v_fmamk_f32 v19, v19, 0x3c800000, v193
	v_mul_f32_e32 v26, 0x4f800000, v19
	v_cmp_gt_f32_e32 vcc, s69, v19
	s_nop 1
	v_cndmask_b32_e32 v19, v19, v26, vcc
	v_sqrt_f32_e32 v26, v19
	s_nop 0
	v_add_u32_e32 v27, -1, v26
	v_fma_f32 v28, -v27, v26, v19
	v_cmp_ge_f32_e64 s[6:7], 0, v28
	v_add_u32_e32 v28, 1, v26
	s_nop 0
	v_cndmask_b32_e64 v27, v26, v27, s[6:7]
	v_fma_f32 v26, -v28, v26, v19
	v_cmp_lt_f32_e64 s[6:7], 0, v26
	s_nop 1
	v_cndmask_b32_e64 v26, v27, v28, s[6:7]
	v_mul_f32_e32 v27, 0x37800000, v26
	v_cndmask_b32_e32 v26, v26, v27, vcc
	v_cmp_class_f32_e32 vcc, v19, v194
	s_nop 1
	v_cndmask_b32_e32 v19, v26, v19, vcc
	v_div_scale_f32 v26, s[6:7], v19, v19, 1.0
	v_rcp_f32_e32 v27, v26
	s_nop 0
	v_fma_f32 v28, -v26, v27, 1.0
	v_fmac_f32_e32 v27, v28, v27
	v_div_scale_f32 v28, vcc, 1.0, v19, 1.0
	v_mul_f32_e32 v29, v28, v27
	v_fma_f32 v30, -v26, v29, v28
	v_fmac_f32_e32 v29, v30, v27
	v_fma_f32 v26, -v26, v29, v28
	v_div_fmas_f32 v26, v26, v27, v29
	v_div_fixup_f32 v28, v26, v19, 1.0
	v_pk_mul_f32 v[26:27], v[62:63], v[28:29] op_sel_hi:[1,0]
	v_pk_mul_f32 v[30:31], v[64:65], v[28:29] op_sel_hi:[1,0]
	s_nop 0
	v_pk_mul_f32 v[182:183], v[14:15], v[26:27]
	v_pk_mul_f32 v[178:179], v[16:17], v[30:31]
	v_pk_mul_f32 v[26:27], v[58:59], v[28:29] op_sel_hi:[1,0]
	v_pk_mul_f32 v[30:31], v[60:61], v[28:29] op_sel_hi:[1,0]
	v_pk_mul_f32 v[184:185], v[6:7], v[26:27]
	v_pk_mul_f32 v[180:181], v[8:9], v[30:31]
	v_pk_mul_f32 v[30:31], v[54:55], v[28:29] op_sel_hi:[1,0]
	v_pk_mul_f32 v[26:27], v[56:57], v[28:29] op_sel_hi:[1,0]
	v_pk_mul_f32 v[32:33], v[50:51], v[28:29] op_sel_hi:[1,0]
	v_pk_mul_f32 v[28:29], v[52:53], v[28:29] op_sel_hi:[1,0]
	v_pk_mul_f32 v[26:27], v[12:13], v[26:27]
	v_pk_mul_f32 v[30:31], v[10:11], v[30:31]
	v_pk_mul_f32 v[28:29], v[4:5], v[28:29]
	v_pk_mul_f32 v[32:33], v[2:3], v[32:33]
; template <bool F8OUT = false> __device__ __forceinline__ void head_tile_store(const f32x4 (&acc)[2][2][4][2], bf16_t* obase  , int opitch, const float* gain, float scale, const f32x2e* rope, int row0, int fq) {
;     ...
;             const int row = row0 + ai * HALF + m * 16;
;             f32x4 x[2][2];
; #pragma unroll
;             for (int bj = 0; bj < 2; ++bj)
; #pragma unroll
;                 for (int n = 0; n < 2; ++n) x[bj][n] = acc[ai][bj][m][n];
;             if (gain) {
;                 float ss = 0.f;
; #pragma unroll
;                 for (int bj = 0; bj < 2; ++bj)
; #pragma unroll
;                     for (int n = 0; n < 2; ++n) ss += (x[bj][n][0] * x[bj][n][0] + x[bj][n][1] * x[bj][n][1]) + (x[bj][n][2] * x[bj][n][2] + x[bj][n][3] * x[bj][n][3]);
;                 ss += __shfl_xor(ss, 16); ss += __shfl_xor(ss, 32);
;                 const float r = scale / sqrtf(ss * (1.f / 64.f) + 1e-6f);
; #pragma unroll
;                 for (int bj = 0; bj < 2; ++bj)
; #pragma unroll
;                     for (int n = 0; n < 2; ++n) x[bj][n] = x[bj][n] * r * g[bj][n];
;             }
;             if (rope) {
;                 const int t = row & 8191; const bool second = (fq & 2) != 0;
; #pragma unroll
;                 for (int bj = 0; bj < 2; ++bj) { const int pos = bj ? (t & 63) : (t >> 6); const f32x2e* tb = rope + pos * 16 + 8 * (fq & 1);
; #pragma unroll
;                     for (int n = 0; n < 2; ++n)
; #pragma unroll
;                         for (int e = 0; e < 4; ++e) { const float p = __shfl_xor(x[bj][n][e], 32); const f32x2e cs = tb[4 * n + e]; const float v = x[bj][n][e];
;                             x[bj][n][e] = second ? (p * cs.y + v * cs.x) : (v * cs.x - p * cs.y); } }
;             }
;             if constexpr (F8OUT) { unsigned char* rowp8 = (unsigned char*)obase + (size_t)row * opitch + 8 * fq; typedef unsigned u32x2_ __attribute__((ext_vector_type(2)));
; #pragma unroll
;                 for (int bj = 0; bj < 2; ++bj) *(u32x2_*)(rowp8 + 32 * bj) = (u32x2_){pk4_fp8(x[bj][0][0], x[bj][0][1], x[bj][0][2], x[bj][0][3]), pk4_fp8(x[bj][1][0], x[bj][1][1], x[bj][1][2], x[bj][1][3])};
;                 continue; }
;             bf16_t* rowp = obase + (size_t)row * opitch + 8 * fq;
; #pragma unroll
.LBB0_1049:
	v_lshl_add_u64 v[196:197], v[24:25], 0, s[38:39]
	v_add_co_u32_e32 v24, vcc, 0x14000, v24
	v_cvt_pk_bf16_f32 v182, v182, v183
	v_cvt_pk_bf16_f32 v183, v178, v179
	v_cvt_pk_bf16_f32 v184, v184, v185
	v_cvt_pk_bf16_f32 v185, v180, v181
	s_nop 1
	v_addc_co_u32_e32 v25, vcc, 0, v25, vcc
	global_store_dwordx4 v[24:25], v[182:185], off
	v_cvt_pk_bf16_f32 v24, v30, v31
	v_cvt_pk_bf16_f32 v25, v26, v27
	v_cvt_pk_bf16_f32 v26, v32, v33
	v_cvt_pk_bf16_f32 v27, v28, v29
	global_store_dwordx4 v[196:197], v[24:27], off offset:64
	s_and_b64 vcc, exec, s[4:5]
	v_mov_b32_e32 v29, v35
	v_mov_b32_e32 v25, v37
	v_mov_b32_e32 v24, v36
	v_mov_b32_e32 v28, v34
	v_mov_b32_e32 v27, v41
	v_mov_b32_e32 v26, v40
	v_mov_b32_e32 v31, v39
	v_mov_b32_e32 v30, v38
	v_mov_b32_e32 v33, v45
	v_mov_b32_e32 v32, v44
	v_mov_b32_e32 v181, v43
	v_mov_b32_e32 v180, v42
	v_mov_b32_e32 v179, v49
	v_mov_b32_e32 v178, v48
	v_mov_b32_e32 v183, v47
	v_mov_b32_e32 v182, v46
	s_cbranch_vccnz .LBB0_1051
	v_pk_mul_f32 v[24:25], v[48:49], v[48:49]
	v_pk_mul_f32 v[26:27], v[46:47], v[46:47]
	v_mul_f32_e32 v19, v34, v34
	v_pk_mov_b32 v[28:29], v[26:27], v[24:25] op_sel:[1,0]
	v_mov_b32_e32 v27, v25
	v_pk_add_f32 v[24:25], v[28:29], v[26:27]
	v_pk_mul_f32 v[26:27], v[44:45], v[44:45]
	v_pk_mul_f32 v[28:29], v[42:43], v[42:43]
	v_pk_add_f32 v[24:25], v[24:25], v[24:25] op_sel:[0,1] op_sel_hi:[1,0]
	v_pk_mov_b32 v[30:31], v[28:29], v[26:27] op_sel:[1,0]
	v_mov_b32_e32 v29, v27
	v_pk_add_f32 v[26:27], v[30:31], v[28:29]
	v_mul_f32_e32 v28, v35, v35
	v_pk_add_f32 v[26:27], v[26:27], v[26:27] op_sel:[0,1] op_sel_hi:[1,0]
	v_mov_b32_e32 v25, v19
	v_mov_b32_e32 v27, v28
	v_pk_add_f32 v[24:25], v[24:25], v[26:27]
	v_mul_f32_e32 v26, v39, v39
	v_mul_f32_e32 v29, v36, v36
	v_pk_fma_f32 v[26:27], v[38:39], v[38:39], v[26:27] op_sel_hi:[1,1,0]
	v_mul_f32_e32 v28, v41, v41
	v_mul_f32_e32 v30, v37, v37
	v_mov_b32_e32 v27, v29
	v_pk_fma_f32 v[28:29], v[40:41], v[40:41], v[28:29] op_sel_hi:[1,1,0]
	s_nop 0
	v_mov_b32_e32 v29, v30
	v_pk_add_f32 v[26:27], v[26:27], v[28:29]
	s_nop 0
	v_pk_add_f32 v[24:25], v[24:25], v[26:27]
	s_nop 0
	v_add_f32_e32 v19, v24, v25
	v_and_b32_e32 v25, 64, v195
	v_xor_b32_e32 v24, 16, v195
	v_add_u32_e32 v25, 64, v25
	v_cmp_lt_i32_e32 vcc, v24, v25
	s_nop 1
	v_cndmask_b32_e32 v24, v195, v24, vcc
	v_lshlrev_b32_e32 v24, 2, v24
	ds_bpermute_b32 v24, v24, v19
	s_waitcnt lgkmcnt(0)
	v_add_f32_e32 v19, v19, v24
	v_xor_b32_e32 v24, 32, v195
	v_cmp_lt_i32_e32 vcc, v24, v25
	s_nop 1
	v_cndmask_b32_e32 v24, v195, v24, vcc
	v_lshlrev_b32_e32 v24, 2, v24
	ds_bpermute_b32 v24, v24, v19
	s_waitcnt lgkmcnt(0)
	v_add_f32_e32 v19, v19, v24
	v_fmamk_f32 v19, v19, 0x3c800000, v193
	v_mul_f32_e32 v24, 0x4f800000, v19
	v_cmp_gt_f32_e32 vcc, s69, v19
	s_nop 1
	v_cndmask_b32_e32 v19, v19, v24, vcc
	v_sqrt_f32_e32 v24, v19
	s_nop 0
	v_add_u32_e32 v25, -1, v24
	v_fma_f32 v26, -v25, v24, v19
	v_cmp_ge_f32_e64 s[4:5], 0, v26
	v_add_u32_e32 v26, 1, v24
	s_nop 0
	v_cndmask_b32_e64 v25, v24, v25, s[4:5]
	v_fma_f32 v24, -v26, v24, v19
	v_cmp_lt_f32_e64 s[4:5], 0, v24
	s_nop 1
	v_cndmask_b32_e64 v24, v25, v26, s[4:5]
	v_mul_f32_e32 v25, 0x37800000, v24
	v_cndmask_b32_e32 v24, v24, v25, vcc
	v_cmp_class_f32_e32 vcc, v19, v194
	s_nop 1
	v_cndmask_b32_e32 v19, v24, v19, vcc
	v_div_scale_f32 v24, s[4:5], v19, v19, 1.0
	v_rcp_f32_e32 v25, v24
	s_nop 0
	v_fma_f32 v26, -v24, v25, 1.0
	v_fmac_f32_e32 v25, v26, v25
	v_div_scale_f32 v26, vcc, 1.0, v19, 1.0
	v_mul_f32_e32 v27, v26, v25
	v_fma_f32 v28, -v24, v27, v26
	v_fmac_f32_e32 v27, v28, v25
	v_fma_f32 v24, -v24, v27, v26
	v_div_fmas_f32 v24, v24, v25, v27
	v_div_fixup_f32 v24, v24, v19, 1.0
	v_pk_mul_f32 v[26:27], v[46:47], v[24:25] op_sel_hi:[1,0]
	v_pk_mul_f32 v[28:29], v[48:49], v[24:25] op_sel_hi:[1,0]
	s_nop 0
	v_pk_mul_f32 v[182:183], v[14:15], v[26:27]
	v_pk_mul_f32 v[178:179], v[16:17], v[28:29]
	v_pk_mul_f32 v[14:15], v[42:43], v[24:25] op_sel_hi:[1,0]
	v_pk_mul_f32 v[16:17], v[44:45], v[24:25] op_sel_hi:[1,0]
	v_pk_mul_f32 v[180:181], v[6:7], v[14:15]
	v_pk_mul_f32 v[32:33], v[8:9], v[16:17]
	v_pk_mul_f32 v[6:7], v[38:39], v[24:25] op_sel_hi:[1,0]
	v_pk_mul_f32 v[8:9], v[40:41], v[24:25] op_sel_hi:[1,0]
	v_pk_mul_f32 v[30:31], v[10:11], v[6:7]
	v_pk_mul_f32 v[26:27], v[12:13], v[8:9]
	v_pk_mul_f32 v[6:7], v[34:35], v[24:25] op_sel_hi:[1,0]
	v_pk_mul_f32 v[8:9], v[36:37], v[24:25] op_sel_hi:[1,0]
	v_pk_mul_f32 v[28:29], v[2:3], v[6:7]
	v_pk_mul_f32 v[24:25], v[4:5], v[8:9]
.LBB0_1051:
	s_nop 0
	v_lshlrev_b64 v[2:3], 9, v[20:21]
	v_lshl_add_u64 v[8:9], v[22:23], 0, v[2:3]
	v_lshl_add_u64 v[6:7], v[8:9], 0, s[40:41]
	v_add_co_u32_e32 v8, vcc, s61, v8
	v_cvt_pk_bf16_f32 v2, v182, v183
	v_cvt_pk_bf16_f32 v3, v178, v179
	v_cvt_pk_bf16_f32 v4, v180, v181
	v_cvt_pk_bf16_f32 v5, v32, v33
	s_nop 1
	v_addc_co_u32_e32 v9, vcc, 0, v9, vcc
	global_store_dwordx4 v[8:9], v[2:5], off
	s_nop 1
	v_cvt_pk_bf16_f32 v2, v30, v31
	v_cvt_pk_bf16_f32 v3, v26, v27
	v_cvt_pk_bf16_f32 v4, v28, v29
	v_cvt_pk_bf16_f32 v5, v24, v25

; template <bool F8OUT = false> __device__ __forceinline__ void head_tile_store(const f32x4 (&acc)[2][2][4][2], bf16_t* obase  , int opitch, const float* gain, float scale, const f32x2e* rope, int row0, int fq) {
;     ...
;             const int row = row0 + ai * HALF + m * 16;
;             f32x4 x[2][2];
; #pragma unroll
;             for (int bj = 0; bj < 2; ++bj)
; #pragma unroll
;                 for (int n = 0; n < 2; ++n) x[bj][n] = acc[ai][bj][m][n];
;             if (gain) {
;                 float ss = 0.f;
; #pragma unroll
;                 for (int bj = 0; bj < 2; ++bj)
; #pragma unroll
;                     for (int n = 0; n < 2; ++n) ss += (x[bj][n][0] * x[bj][n][0] + x[bj][n][1] * x[bj][n][1]) + (x[bj][n][2] * x[bj][n][2] + x[bj][n][3] * x[bj][n][3]);
;                 ss += __shfl_xor(ss, 16); ss += __shfl_xor(ss, 32);
;                 const float r = scale / sqrtf(ss * (1.f / 64.f) + 1e-6f);
; #pragma unroll
;                 for (int bj = 0; bj < 2; ++bj)
; #pragma unroll
;                     for (int n = 0; n < 2; ++n) x[bj][n] = x[bj][n] * r * g[bj][n];
;             }
;             if (rope) {
;                 const int t = row & 8191; const bool second = (fq & 2) != 0;
; #pragma unroll
;                 for (int bj = 0; bj < 2; ++bj) { const int pos = bj ? (t & 63) : (t >> 6); const f32x2e* tb = rope + pos * 16 + 8 * (fq & 1);
; #pragma unroll
;                     for (int n = 0; n < 2; ++n)
; #pragma unroll
;                         for (int e = 0; e < 4; ++e) { const float p = __shfl_xor(x[bj][n][e], 32); const f32x2e cs = tb[4 * n + e]; const float v = x[bj][n][e];
;                             x[bj][n][e] = second ? (p * cs.y + v * cs.x) : (v * cs.x - p * cs.y); } }
;             }
;             if constexpr (F8OUT) { unsigned char* rowp8 = (unsigned char*)obase + (size_t)row * opitch + 8 * fq; typedef unsigned u32x2_ __attribute__((ext_vector_type(2)));
; #pragma unroll
;                 for (int bj = 0; bj < 2; ++bj) *(u32x2_*)(rowp8 + 32 * bj) = (u32x2_){pk4_fp8(x[bj][0][0], x[bj][0][1], x[bj][0][2], x[bj][0][3]), pk4_fp8(x[bj][1][0], x[bj][1][1], x[bj][1][2], x[bj][1][3])};
;                 continue; }
;             bf16_t* rowp = obase + (size_t)row * opitch + 8 * fq;
; #pragma unroll
.LBB0_1059:
	s_lshl_b32 s6, s50, 8
	s_or_b32 s6, s6, s66
	s_ashr_i32 s7, s6, 31
	s_lshl_b64 s[6:7], s[6:7], 1
	v_readlane_b32 s52, v255, 7
	v_readlane_b32 s53, v255, 8
	s_add_u32 s6, s52, s6
	s_addc_u32 s7, s53, s7
	v_ashrrev_i32_e32 v19, 31, v18
	v_lshl_add_u64 v[20:21], v[20:21], 1, s[6:7]
	v_lshlrev_b64 v[22:23], 11, v[18:19]
	v_lshl_add_u64 v[22:23], v[20:21], 0, v[22:23]
	v_cvt_pk_bf16_f32 v24, v158, v159
	v_cvt_pk_bf16_f32 v25, v160, v161
	v_cvt_pk_bf16_f32 v26, v154, v155
	v_cvt_pk_bf16_f32 v27, v156, v157
	s_and_b64 vcc, exec, s[4:5]
	global_store_dwordx4 v[22:23], v[24:27], off
	s_nop 1
	v_cvt_pk_bf16_f32 v24, v150, v151
	v_cvt_pk_bf16_f32 v25, v152, v153
	v_cvt_pk_bf16_f32 v26, v146, v147
	v_cvt_pk_bf16_f32 v27, v148, v149
	global_store_dwordx4 v[22:23], v[24:27], off offset:64
	s_cbranch_vccnz .LBB0_1061
	s_nop 0
	v_pk_mul_f32 v[24:25], v[144:145], v[144:145]
	v_pk_mul_f32 v[26:27], v[142:143], v[142:143]
	s_nop 0
	v_pk_mov_b32 v[28:29], v[26:27], v[24:25] op_sel:[1,0]
	v_mov_b32_e32 v27, v25
	v_pk_add_f32 v[24:25], v[28:29], v[26:27]
	v_pk_mul_f32 v[26:27], v[140:141], v[140:141]
	v_pk_mul_f32 v[28:29], v[138:139], v[138:139]
	v_pk_add_f32 v[24:25], v[24:25], v[24:25] op_sel:[0,1] op_sel_hi:[1,0]
	v_pk_mov_b32 v[30:31], v[28:29], v[26:27] op_sel:[1,0]
	v_mov_b32_e32 v29, v27
	v_pk_add_f32 v[26:27], v[30:31], v[28:29]
	v_mul_f32_e32 v28, v130, v130
	v_mul_f32_e32 v29, v131, v131
	v_pk_add_f32 v[26:27], v[26:27], v[26:27] op_sel:[0,1] op_sel_hi:[1,0]
	v_mov_b32_e32 v25, v28
	v_mov_b32_e32 v27, v29
	v_pk_add_f32 v[24:25], v[24:25], v[26:27]
	v_mul_f32_e32 v26, v135, v135
	v_mul_f32_e32 v28, v137, v137
	v_mul_f32_e32 v30, v132, v132
	v_mul_f32_e32 v31, v133, v133
	v_pk_fma_f32 v[26:27], v[134:135], v[134:135], v[26:27] op_sel_hi:[1,1,0]
	v_pk_fma_f32 v[28:29], v[136:137], v[136:137], v[28:29] op_sel_hi:[1,1,0]
	v_mov_b32_e32 v27, v30
	v_mov_b32_e32 v29, v31
	v_pk_add_f32 v[26:27], v[26:27], v[28:29]
	s_nop 0
	v_pk_add_f32 v[24:25], v[24:25], v[26:27]
	v_and_b32_e32 v26, 64, v195
	v_add_f32_e32 v24, v24, v25
	v_xor_b32_e32 v25, 16, v195
	v_add_u32_e32 v26, 64, v26
	v_cmp_lt_i32_e32 vcc, v25, v26
	s_nop 1
	v_cndmask_b32_e32 v25, v195, v25, vcc
	v_lshlrev_b32_e32 v25, 2, v25
	ds_bpermute_b32 v25, v25, v24
	s_waitcnt lgkmcnt(0)
	v_add_f32_e32 v24, v24, v25
	v_xor_b32_e32 v25, 32, v195
	v_cmp_lt_i32_e32 vcc, v25, v26
	s_nop 1
	v_cndmask_b32_e32 v25, v195, v25, vcc
	v_lshlrev_b32_e32 v25, 2, v25
	ds_bpermute_b32 v25, v25, v24
	s_waitcnt lgkmcnt(0)
	v_add_f32_e32 v24, v24, v25
	v_fmamk_f32 v24, v24, 0x3c800000, v193
	v_mul_f32_e32 v25, 0x4f800000, v24
	v_cmp_gt_f32_e32 vcc, s69, v24
	s_nop 1
	v_cndmask_b32_e32 v24, v24, v25, vcc
	v_sqrt_f32_e32 v25, v24
	s_nop 0
	v_add_u32_e32 v26, -1, v25
	v_fma_f32 v27, -v26, v25, v24
	v_cmp_ge_f32_e64 s[6:7], 0, v27
	v_add_u32_e32 v27, 1, v25
	s_nop 0
	v_cndmask_b32_e64 v26, v25, v26, s[6:7]
	v_fma_f32 v25, -v27, v25, v24
	v_cmp_lt_f32_e64 s[6:7], 0, v25
	s_nop 1
	v_cndmask_b32_e64 v25, v26, v27, s[6:7]
	v_mul_f32_e32 v26, 0x37800000, v25
	v_cndmask_b32_e32 v25, v25, v26, vcc
	v_cmp_class_f32_e32 vcc, v24, v194
	s_nop 1
	v_cndmask_b32_e32 v24, v25, v24, vcc
	v_div_scale_f32 v25, s[6:7], v24, v24, s70
	v_rcp_f32_e32 v26, v25
	s_nop 0
	v_fma_f32 v27, -v25, v26, 1.0
	v_fmac_f32_e32 v26, v27, v26
	v_div_scale_f32 v27, vcc, s70, v24, s70
	v_mul_f32_e32 v28, v27, v26
	v_fma_f32 v29, -v25, v28, v27
	v_fmac_f32_e32 v28, v29, v26
	v_fma_f32 v25, -v25, v28, v27
	v_div_fmas_f32 v25, v25, v26, v28
	v_div_fixup_f32 v24, v25, v24, s70
	v_pk_mul_f32 v[26:27], v[142:143], v[24:25] op_sel_hi:[1,0]
	v_pk_mul_f32 v[28:29], v[144:145], v[24:25] op_sel_hi:[1,0]
	s_nop 0
	v_pk_mul_f32 v[142:143], v[14:15], v[26:27]
	v_pk_mul_f32 v[26:27], v[138:139], v[24:25] op_sel_hi:[1,0]
	v_pk_mul_f32 v[144:145], v[16:17], v[28:29]
	v_pk_mul_f32 v[28:29], v[140:141], v[24:25] op_sel_hi:[1,0]
	v_pk_mul_f32 v[138:139], v[6:7], v[26:27]
	v_pk_mul_f32 v[26:27], v[134:135], v[24:25] op_sel_hi:[1,0]
	v_pk_mul_f32 v[140:141], v[8:9], v[28:29]
	v_pk_mul_f32 v[28:29], v[136:137], v[24:25] op_sel_hi:[1,0]
	v_pk_mul_f32 v[134:135], v[10:11], v[26:27]
	v_pk_mul_f32 v[26:27], v[130:131], v[24:25] op_sel_hi:[1,0]
	v_pk_mul_f32 v[24:25], v[132:133], v[24:25] op_sel_hi:[1,0]
	v_pk_mul_f32 v[136:137], v[12:13], v[28:29]
	v_pk_mul_f32 v[132:133], v[4:5], v[24:25]
	v_pk_mul_f32 v[130:131], v[2:3], v[26:27]
; template <bool F8OUT = false> __device__ __forceinline__ void head_tile_store(const f32x4 (&acc)[2][2][4][2], bf16_t* obase  , int opitch, const float* gain, float scale, const f32x2e* rope, int row0, int fq) {
;     ...
;             const int row = row0 + ai * HALF + m * 16;
;             f32x4 x[2][2];
; #pragma unroll
;             for (int bj = 0; bj < 2; ++bj)
; #pragma unroll
;                 for (int n = 0; n < 2; ++n) x[bj][n] = acc[ai][bj][m][n];
;             if (gain) {
;                 float ss = 0.f;
; #pragma unroll
;                 for (int bj = 0; bj < 2; ++bj)
; #pragma unroll
;                     for (int n = 0; n < 2; ++n) ss += (x[bj][n][0] * x[bj][n][0] + x[bj][n][1] * x[bj][n][1]) + (x[bj][n][2] * x[bj][n][2] + x[bj][n][3] * x[bj][n][3]);
;                 ss += __shfl_xor(ss, 16); ss += __shfl_xor(ss, 32);
;                 const float r = scale / sqrtf(ss * (1.f / 64.f) + 1e-6f);
; #pragma unroll
;                 for (int bj = 0; bj < 2; ++bj)
; #pragma unroll
;                     for (int n = 0; n < 2; ++n) x[bj][n] = x[bj][n] * r * g[bj][n];
;             }
;             if (rope) {
;                 const int t = row & 8191; const bool second = (fq & 2) != 0;
; #pragma unroll
;                 for (int bj = 0; bj < 2; ++bj) { const int pos = bj ? (t & 63) : (t >> 6); const f32x2e* tb = rope + pos * 16 + 8 * (fq & 1);
; #pragma unroll
;                     for (int n = 0; n < 2; ++n)
; #pragma unroll
;                         for (int e = 0; e < 4; ++e) { const float p = __shfl_xor(x[bj][n][e], 32); const f32x2e cs = tb[4 * n + e]; const float v = x[bj][n][e];
;                             x[bj][n][e] = second ? (p * cs.y + v * cs.x) : (v * cs.x - p * cs.y); } }
;             }
;             if constexpr (F8OUT) { unsigned char* rowp8 = (unsigned char*)obase + (size_t)row * opitch + 8 * fq; typedef unsigned u32x2_ __attribute__((ext_vector_type(2)));
; #pragma unroll
;                 for (int bj = 0; bj < 2; ++bj) *(u32x2_*)(rowp8 + 32 * bj) = (u32x2_){pk4_fp8(x[bj][0][0], x[bj][0][1], x[bj][0][2], x[bj][0][3]), pk4_fp8(x[bj][1][0], x[bj][1][1], x[bj][1][2], x[bj][1][3])};
;                 continue; }
;             bf16_t* rowp = obase + (size_t)row * opitch + 8 * fq;
; #pragma unroll
.LBB0_1061:
	v_add_co_u32_e32 v30, vcc, 0x8000, v22
	s_mov_b64 s[6:7], 0x8000
	s_nop 0
	v_addc_co_u32_e32 v31, vcc, 0, v23, vcc
	v_lshl_add_u64 v[28:29], v[22:23], 0, s[6:7]
	v_cvt_pk_bf16_f32 v24, v142, v143
	v_cvt_pk_bf16_f32 v25, v144, v145
	v_cvt_pk_bf16_f32 v26, v138, v139
	v_cvt_pk_bf16_f32 v27, v140, v141
	s_and_b64 vcc, exec, s[4:5]
	global_store_dwordx4 v[30:31], v[24:27], off
	s_nop 1
	v_cvt_pk_bf16_f32 v24, v134, v135
	v_cvt_pk_bf16_f32 v25, v136, v137
	v_cvt_pk_bf16_f32 v26, v130, v131
	v_cvt_pk_bf16_f32 v27, v132, v133
	global_store_dwordx4 v[28:29], v[24:27], off offset:64
	s_cbranch_vccnz .LBB0_1063
	s_nop 0
	v_pk_mul_f32 v[24:25], v[128:129], v[128:129]
	v_pk_mul_f32 v[26:27], v[126:127], v[126:127]
	s_nop 0
	v_pk_mov_b32 v[28:29], v[26:27], v[24:25] op_sel:[1,0]
	v_mov_b32_e32 v27, v25
	v_pk_add_f32 v[24:25], v[28:29], v[26:27]
	v_pk_mul_f32 v[26:27], v[124:125], v[124:125]
	v_pk_mul_f32 v[28:29], v[122:123], v[122:123]
	v_pk_add_f32 v[24:25], v[24:25], v[24:25] op_sel:[0,1] op_sel_hi:[1,0]
	v_pk_mov_b32 v[30:31], v[28:29], v[26:27] op_sel:[1,0]
	v_mov_b32_e32 v29, v27
	v_pk_add_f32 v[26:27], v[30:31], v[28:29]
	v_mul_f32_e32 v28, v114, v114
	v_mul_f32_e32 v29, v115, v115
	v_pk_add_f32 v[26:27], v[26:27], v[26:27] op_sel:[0,1] op_sel_hi:[1,0]
	v_mov_b32_e32 v25, v28
	v_mov_b32_e32 v27, v29
	v_pk_add_f32 v[24:25], v[24:25], v[26:27]
	v_mul_f32_e32 v26, v119, v119
	v_mul_f32_e32 v28, v121, v121
	v_mul_f32_e32 v30, v116, v116
	v_mul_f32_e32 v31, v117, v117
	v_pk_fma_f32 v[26:27], v[118:119], v[118:119], v[26:27] op_sel_hi:[1,1,0]
	v_pk_fma_f32 v[28:29], v[120:121], v[120:121], v[28:29] op_sel_hi:[1,1,0]
	v_mov_b32_e32 v27, v30
	v_mov_b32_e32 v29, v31
	v_pk_add_f32 v[26:27], v[26:27], v[28:29]
	s_nop 0
	v_pk_add_f32 v[24:25], v[24:25], v[26:27]
	v_and_b32_e32 v26, 64, v195
	v_add_f32_e32 v24, v24, v25
	v_xor_b32_e32 v25, 16, v195
	v_add_u32_e32 v26, 64, v26
	v_cmp_lt_i32_e32 vcc, v25, v26
	s_nop 1
	v_cndmask_b32_e32 v25, v195, v25, vcc
	v_lshlrev_b32_e32 v25, 2, v25
	ds_bpermute_b32 v25, v25, v24
	s_waitcnt lgkmcnt(0)
	v_add_f32_e32 v24, v24, v25
	v_xor_b32_e32 v25, 32, v195
	v_cmp_lt_i32_e32 vcc, v25, v26
	s_nop 1
	v_cndmask_b32_e32 v25, v195, v25, vcc
	v_lshlrev_b32_e32 v25, 2, v25
	ds_bpermute_b32 v25, v25, v24
	s_waitcnt lgkmcnt(0)
	v_add_f32_e32 v24, v24, v25
	v_fmamk_f32 v24, v24, 0x3c800000, v193
	v_mul_f32_e32 v25, 0x4f800000, v24
	v_cmp_gt_f32_e32 vcc, s69, v24
	s_nop 1
	v_cndmask_b32_e32 v24, v24, v25, vcc
	v_sqrt_f32_e32 v25, v24
	s_nop 0
	v_add_u32_e32 v26, -1, v25
	v_fma_f32 v27, -v26, v25, v24
	v_cmp_ge_f32_e64 s[6:7], 0, v27
	v_add_u32_e32 v27, 1, v25
	s_nop 0
	v_cndmask_b32_e64 v26, v25, v26, s[6:7]
	v_fma_f32 v25, -v27, v25, v24
	v_cmp_lt_f32_e64 s[6:7], 0, v25
	s_nop 1
	v_cndmask_b32_e64 v25, v26, v27, s[6:7]
	v_mul_f32_e32 v26, 0x37800000, v25
	v_cndmask_b32_e32 v25, v25, v26, vcc
	v_cmp_class_f32_e32 vcc, v24, v194
	s_nop 1
	v_cndmask_b32_e32 v24, v25, v24, vcc
	v_div_scale_f32 v25, s[6:7], v24, v24, s70
	v_rcp_f32_e32 v26, v25
	s_nop 0
	v_fma_f32 v27, -v25, v26, 1.0
	v_fmac_f32_e32 v26, v27, v26
	v_div_scale_f32 v27, vcc, s70, v24, s70
	v_mul_f32_e32 v28, v27, v26
	v_fma_f32 v29, -v25, v28, v27
	v_fmac_f32_e32 v28, v29, v26
	v_fma_f32 v25, -v25, v28, v27
	v_div_fmas_f32 v25, v25, v26, v28
	v_div_fixup_f32 v24, v25, v24, s70
	v_pk_mul_f32 v[26:27], v[126:127], v[24:25] op_sel_hi:[1,0]
	v_pk_mul_f32 v[28:29], v[128:129], v[24:25] op_sel_hi:[1,0]
	s_nop 0
	v_pk_mul_f32 v[126:127], v[14:15], v[26:27]
	v_pk_mul_f32 v[26:27], v[122:123], v[24:25] op_sel_hi:[1,0]
	v_pk_mul_f32 v[128:129], v[16:17], v[28:29]
	v_pk_mul_f32 v[28:29], v[124:125], v[24:25] op_sel_hi:[1,0]
	v_pk_mul_f32 v[122:123], v[6:7], v[26:27]
	v_pk_mul_f32 v[26:27], v[118:119], v[24:25] op_sel_hi:[1,0]
	v_pk_mul_f32 v[124:125], v[8:9], v[28:29]
	v_pk_mul_f32 v[28:29], v[120:121], v[24:25] op_sel_hi:[1,0]
	v_pk_mul_f32 v[118:119], v[10:11], v[26:27]
	v_pk_mul_f32 v[26:27], v[114:115], v[24:25] op_sel_hi:[1,0]
	v_pk_mul_f32 v[24:25], v[116:117], v[24:25] op_sel_hi:[1,0]
	v_pk_mul_f32 v[120:121], v[12:13], v[28:29]
	v_pk_mul_f32 v[116:117], v[4:5], v[24:25]
	v_pk_mul_f32 v[114:115], v[2:3], v[26:27]
.LBB0_1063:
	v_lshl_add_u64 v[28:29], v[22:23], 0, s[34:35]
	v_add_co_u32_e32 v22, vcc, 0x10000, v22
	v_cvt_pk_bf16_f32 v24, v126, v127
	v_cvt_pk_bf16_f32 v25, v128, v129
	v_cvt_pk_bf16_f32 v26, v122, v123
	v_cvt_pk_bf16_f32 v27, v124, v125
	s_nop 1
	v_addc_co_u32_e32 v23, vcc, 0, v23, vcc
	s_and_b64 vcc, exec, s[4:5]
	global_store_dwordx4 v[22:23], v[24:27], off
	v_cvt_pk_bf16_f32 v22, v118, v119
	v_cvt_pk_bf16_f32 v23, v120, v121
	s_nop 1
	v_cvt_pk_bf16_f32 v24, v114, v115
	v_cvt_pk_bf16_f32 v25, v116, v117
	global_store_dwordx4 v[28:29], v[22:25], off offset:64
	s_cbranch_vccnz .LBB0_1065
; template <bool F8OUT = false> __device__ __forceinline__ void head_tile_store(const f32x4 (&acc)[2][2][4][2], bf16_t* obase  , int opitch, const float* gain, float scale, const f32x2e* rope, int row0, int fq) {
;     ...
;             const int row = row0 + ai * HALF + m * 16;
;             f32x4 x[2][2];
; #pragma unroll
;             for (int bj = 0; bj < 2; ++bj)
; #pragma unroll
;                 for (int n = 0; n < 2; ++n) x[bj][n] = acc[ai][bj][m][n];
;             if (gain) {
;                 float ss = 0.f;
; #pragma unroll
;                 for (int bj = 0; bj < 2; ++bj)
; #pragma unroll
;                     for (int n = 0; n < 2; ++n) ss += (x[bj][n][0] * x[bj][n][0] + x[bj][n][1] * x[bj][n][1]) + (x[bj][n][2] * x[bj][n][2] + x[bj][n][3] * x[bj][n][3]);
;                 ss += __shfl_xor(ss, 16); ss += __shfl_xor(ss, 32);
;                 const float r = scale / sqrtf(ss * (1.f / 64.f) + 1e-6f);
; #pragma unroll
;                 for (int bj = 0; bj < 2; ++bj)
; #pragma unroll
;                     for (int n = 0; n < 2; ++n) x[bj][n] = x[bj][n] * r * g[bj][n];
;             }
;             if (rope) {
;                 const int t = row & 8191; const bool second = (fq & 2) != 0;
; #pragma unroll
;                 for (int bj = 0; bj < 2; ++bj) { const int pos = bj ? (t & 63) : (t >> 6); const f32x2e* tb = rope + pos * 16 + 8 * (fq & 1);
; #pragma unroll
;                     for (int n = 0; n < 2; ++n)
; #pragma unroll
;                         for (int e = 0; e < 4; ++e) { const float p = __shfl_xor(x[bj][n][e], 32); const f32x2e cs = tb[4 * n + e]; const float v = x[bj][n][e];
;                             x[bj][n][e] = second ? (p * cs.y + v * cs.x) : (v * cs.x - p * cs.y); } }
;             }
;             if constexpr (F8OUT) { unsigned char* rowp8 = (unsigned char*)obase + (size_t)row * opitch + 8 * fq; typedef unsigned u32x2_ __attribute__((ext_vector_type(2)));
; #pragma unroll
;                 for (int bj = 0; bj < 2; ++bj) *(u32x2_*)(rowp8 + 32 * bj) = (u32x2_){pk4_fp8(x[bj][0][0], x[bj][0][1], x[bj][0][2], x[bj][0][3]), pk4_fp8(x[bj][1][0], x[bj][1][1], x[bj][1][2], x[bj][1][3])};
;                 continue; }
;             bf16_t* rowp = obase + (size_t)row * opitch + 8 * fq;
; #pragma unroll
	s_nop 0
	v_pk_mul_f32 v[22:23], v[112:113], v[112:113]
	v_pk_mul_f32 v[24:25], v[110:111], v[110:111]
	s_nop 0
	v_pk_mov_b32 v[26:27], v[24:25], v[22:23] op_sel:[1,0]
	v_mov_b32_e32 v25, v23
	v_pk_add_f32 v[22:23], v[26:27], v[24:25]
	v_pk_mul_f32 v[24:25], v[108:109], v[108:109]
	v_pk_mul_f32 v[26:27], v[106:107], v[106:107]
	v_pk_add_f32 v[22:23], v[22:23], v[22:23] op_sel:[0,1] op_sel_hi:[1,0]
	v_pk_mov_b32 v[28:29], v[26:27], v[24:25] op_sel:[1,0]
	v_mov_b32_e32 v27, v25
	v_pk_add_f32 v[24:25], v[28:29], v[26:27]
	v_mul_f32_e32 v26, v98, v98
	v_mul_f32_e32 v27, v99, v99
	v_pk_add_f32 v[24:25], v[24:25], v[24:25] op_sel:[0,1] op_sel_hi:[1,0]
	v_mov_b32_e32 v23, v26
	v_mov_b32_e32 v25, v27
	v_pk_add_f32 v[22:23], v[22:23], v[24:25]
	v_mul_f32_e32 v24, v103, v103
	v_mul_f32_e32 v26, v105, v105
	v_mul_f32_e32 v28, v100, v100
	v_mul_f32_e32 v29, v101, v101
	v_pk_fma_f32 v[24:25], v[102:103], v[102:103], v[24:25] op_sel_hi:[1,1,0]
	v_pk_fma_f32 v[26:27], v[104:105], v[104:105], v[26:27] op_sel_hi:[1,1,0]
	v_mov_b32_e32 v25, v28
	v_mov_b32_e32 v27, v29
	v_pk_add_f32 v[24:25], v[24:25], v[26:27]
	s_nop 0
	v_pk_add_f32 v[22:23], v[22:23], v[24:25]
	v_and_b32_e32 v24, 64, v195
	v_add_f32_e32 v22, v22, v23
	v_xor_b32_e32 v23, 16, v195
	v_add_u32_e32 v24, 64, v24
	v_cmp_lt_i32_e32 vcc, v23, v24
	s_nop 1
	v_cndmask_b32_e32 v23, v195, v23, vcc
	v_lshlrev_b32_e32 v23, 2, v23
	ds_bpermute_b32 v23, v23, v22
	s_waitcnt lgkmcnt(0)
	v_add_f32_e32 v22, v22, v23
	v_xor_b32_e32 v23, 32, v195
	v_cmp_lt_i32_e32 vcc, v23, v24
	s_nop 1
	v_cndmask_b32_e32 v23, v195, v23, vcc
	v_lshlrev_b32_e32 v23, 2, v23
	ds_bpermute_b32 v23, v23, v22
	s_waitcnt lgkmcnt(0)
	v_add_f32_e32 v22, v22, v23
	v_fmamk_f32 v22, v22, 0x3c800000, v193
	v_mul_f32_e32 v23, 0x4f800000, v22
	v_cmp_gt_f32_e32 vcc, s69, v22
	s_nop 1
	v_cndmask_b32_e32 v22, v22, v23, vcc
	v_sqrt_f32_e32 v23, v22
	s_nop 0
	v_add_u32_e32 v24, -1, v23
	v_fma_f32 v25, -v24, v23, v22
	v_cmp_ge_f32_e64 s[6:7], 0, v25
	v_add_u32_e32 v25, 1, v23
	s_nop 0
	v_cndmask_b32_e64 v24, v23, v24, s[6:7]
	v_fma_f32 v23, -v25, v23, v22
	v_cmp_lt_f32_e64 s[6:7], 0, v23
	s_nop 1
	v_cndmask_b32_e64 v23, v24, v25, s[6:7]
	v_mul_f32_e32 v24, 0x37800000, v23
	v_cndmask_b32_e32 v23, v23, v24, vcc
	v_cmp_class_f32_e32 vcc, v22, v194
	s_nop 1
	v_cndmask_b32_e32 v22, v23, v22, vcc
	v_div_scale_f32 v23, s[6:7], v22, v22, s70
	v_rcp_f32_e32 v24, v23
	s_nop 0
	v_fma_f32 v25, -v23, v24, 1.0
	v_fmac_f32_e32 v24, v25, v24
	v_div_scale_f32 v25, vcc, s70, v22, s70
	v_mul_f32_e32 v26, v25, v24
	v_fma_f32 v27, -v23, v26, v25
	v_fmac_f32_e32 v26, v27, v24
	v_fma_f32 v23, -v23, v26, v25
	v_div_fmas_f32 v23, v23, v24, v26
	v_div_fixup_f32 v22, v23, v22, s70
	v_pk_mul_f32 v[24:25], v[110:111], v[22:23] op_sel_hi:[1,0]
	v_pk_mul_f32 v[26:27], v[112:113], v[22:23] op_sel_hi:[1,0]
	s_nop 0
	v_pk_mul_f32 v[110:111], v[14:15], v[24:25]
	v_pk_mul_f32 v[24:25], v[106:107], v[22:23] op_sel_hi:[1,0]
	v_pk_mul_f32 v[112:113], v[16:17], v[26:27]
	v_pk_mul_f32 v[26:27], v[108:109], v[22:23] op_sel_hi:[1,0]
	v_pk_mul_f32 v[106:107], v[6:7], v[24:25]
	v_pk_mul_f32 v[24:25], v[102:103], v[22:23] op_sel_hi:[1,0]
	v_pk_mul_f32 v[108:109], v[8:9], v[26:27]
	v_pk_mul_f32 v[26:27], v[104:105], v[22:23] op_sel_hi:[1,0]
	v_pk_mul_f32 v[102:103], v[10:11], v[24:25]
	v_pk_mul_f32 v[24:25], v[98:99], v[22:23] op_sel_hi:[1,0]
	v_pk_mul_f32 v[22:23], v[100:101], v[22:23] op_sel_hi:[1,0]
	v_pk_mul_f32 v[104:105], v[12:13], v[26:27]
	v_pk_mul_f32 v[100:101], v[4:5], v[22:23]
	v_pk_mul_f32 v[98:99], v[2:3], v[24:25]
.LBB0_1065:
	s_nop 0
	v_lshlrev_b64 v[22:23], 11, v[18:19]
	v_lshl_add_u64 v[22:23], v[20:21], 0, v[22:23]
	v_add_co_u32_e32 v30, vcc, 0x18000, v22
	s_mov_b64 s[6:7], 0x18000
	s_nop 0
	v_addc_co_u32_e32 v31, vcc, 0, v23, vcc
	v_lshl_add_u64 v[28:29], v[22:23], 0, s[6:7]
	v_cvt_pk_bf16_f32 v24, v110, v111
	v_cvt_pk_bf16_f32 v25, v112, v113
	v_cvt_pk_bf16_f32 v26, v106, v107
	v_cvt_pk_bf16_f32 v27, v108, v109
	s_and_b64 vcc, exec, s[4:5]
	global_store_dwordx4 v[30:31], v[24:27], off
	s_nop 1
	v_cvt_pk_bf16_f32 v24, v102, v103
	v_cvt_pk_bf16_f32 v25, v104, v105
	v_cvt_pk_bf16_f32 v26, v98, v99
	v_cvt_pk_bf16_f32 v27, v100, v101
	global_store_dwordx4 v[28:29], v[24:27], off offset:64
	s_cbranch_vccnz .LBB0_1067
; template <bool F8OUT = false> __device__ __forceinline__ void head_tile_store(const f32x4 (&acc)[2][2][4][2], bf16_t* obase  , int opitch, const float* gain, float scale, const f32x2e* rope, int row0, int fq) {
;     ...
;             const int row = row0 + ai * HALF + m * 16;
;             f32x4 x[2][2];
; #pragma unroll
;             for (int bj = 0; bj < 2; ++bj)
; #pragma unroll
;                 for (int n = 0; n < 2; ++n) x[bj][n] = acc[ai][bj][m][n];
;             if (gain) {
;                 float ss = 0.f;
; #pragma unroll
;                 for (int bj = 0; bj < 2; ++bj)
; #pragma unroll
;                     for (int n = 0; n < 2; ++n) ss += (x[bj][n][0] * x[bj][n][0] + x[bj][n][1] * x[bj][n][1]) + (x[bj][n][2] * x[bj][n][2] + x[bj][n][3] * x[bj][n][3]);
;                 ss += __shfl_xor(ss, 16); ss += __shfl_xor(ss, 32);
;                 const float r = scale / sqrtf(ss * (1.f / 64.f) + 1e-6f);
; #pragma unroll
;                 for (int bj = 0; bj < 2; ++bj)
; #pragma unroll
;                     for (int n = 0; n < 2; ++n) x[bj][n] = x[bj][n] * r * g[bj][n];
;             }
;             if (rope) {
;                 const int t = row & 8191; const bool second = (fq & 2) != 0;
; #pragma unroll
;                 for (int bj = 0; bj < 2; ++bj) { const int pos = bj ? (t & 63) : (t >> 6); const f32x2e* tb = rope + pos * 16 + 8 * (fq & 1);
; #pragma unroll
;                     for (int n = 0; n < 2; ++n)
; #pragma unroll
;                         for (int e = 0; e < 4; ++e) { const float p = __shfl_xor(x[bj][n][e], 32); const f32x2e cs = tb[4 * n + e]; const float v = x[bj][n][e];
;                             x[bj][n][e] = second ? (p * cs.y + v * cs.x) : (v * cs.x - p * cs.y); } }
;             }
;             if constexpr (F8OUT) { unsigned char* rowp8 = (unsigned char*)obase + (size_t)row * opitch + 8 * fq; typedef unsigned u32x2_ __attribute__((ext_vector_type(2)));
; #pragma unroll
;                 for (int bj = 0; bj < 2; ++bj) *(u32x2_*)(rowp8 + 32 * bj) = (u32x2_){pk4_fp8(x[bj][0][0], x[bj][0][1], x[bj][0][2], x[bj][0][3]), pk4_fp8(x[bj][1][0], x[bj][1][1], x[bj][1][2], x[bj][1][3])};
;                 continue; }
;             bf16_t* rowp = obase + (size_t)row * opitch + 8 * fq;
; #pragma unroll
	s_nop 0
	v_pk_mul_f32 v[24:25], v[96:97], v[96:97]
	v_pk_mul_f32 v[26:27], v[94:95], v[94:95]
	s_nop 0
	v_pk_mov_b32 v[28:29], v[26:27], v[24:25] op_sel:[1,0]
	v_mov_b32_e32 v27, v25
	v_pk_add_f32 v[24:25], v[28:29], v[26:27]
	v_pk_mul_f32 v[26:27], v[92:93], v[92:93]
	v_pk_mul_f32 v[28:29], v[90:91], v[90:91]
	v_pk_add_f32 v[24:25], v[24:25], v[24:25] op_sel:[0,1] op_sel_hi:[1,0]
	v_pk_mov_b32 v[30:31], v[28:29], v[26:27] op_sel:[1,0]
	v_mov_b32_e32 v29, v27
	v_pk_add_f32 v[26:27], v[30:31], v[28:29]
	v_mul_f32_e32 v28, v82, v82
	v_mul_f32_e32 v29, v83, v83
	v_pk_add_f32 v[26:27], v[26:27], v[26:27] op_sel:[0,1] op_sel_hi:[1,0]
	v_mov_b32_e32 v25, v28
	v_mov_b32_e32 v27, v29
	v_pk_add_f32 v[24:25], v[24:25], v[26:27]
	v_mul_f32_e32 v26, v87, v87
	v_mul_f32_e32 v28, v89, v89
	v_mul_f32_e32 v30, v84, v84
	v_mul_f32_e32 v31, v85, v85
	v_pk_fma_f32 v[26:27], v[86:87], v[86:87], v[26:27] op_sel_hi:[1,1,0]
	v_pk_fma_f32 v[28:29], v[88:89], v[88:89], v[28:29] op_sel_hi:[1,1,0]
	v_mov_b32_e32 v27, v30
	v_mov_b32_e32 v29, v31
	v_pk_add_f32 v[26:27], v[26:27], v[28:29]
	s_nop 0
	v_pk_add_f32 v[24:25], v[24:25], v[26:27]
	v_and_b32_e32 v26, 64, v195
	v_add_f32_e32 v24, v24, v25
	v_xor_b32_e32 v25, 16, v195
	v_add_u32_e32 v26, 64, v26
	v_cmp_lt_i32_e32 vcc, v25, v26
	s_nop 1
	v_cndmask_b32_e32 v25, v195, v25, vcc
	v_lshlrev_b32_e32 v25, 2, v25
	ds_bpermute_b32 v25, v25, v24
	s_waitcnt lgkmcnt(0)
	v_add_f32_e32 v24, v24, v25
	v_xor_b32_e32 v25, 32, v195
	v_cmp_lt_i32_e32 vcc, v25, v26
	s_nop 1
	v_cndmask_b32_e32 v25, v195, v25, vcc
	v_lshlrev_b32_e32 v25, 2, v25
	ds_bpermute_b32 v25, v25, v24
	s_waitcnt lgkmcnt(0)
	v_add_f32_e32 v24, v24, v25
	v_fmamk_f32 v24, v24, 0x3c800000, v193
	v_mul_f32_e32 v25, 0x4f800000, v24
	v_cmp_gt_f32_e32 vcc, s69, v24
	s_nop 1
	v_cndmask_b32_e32 v24, v24, v25, vcc
	v_sqrt_f32_e32 v25, v24
	s_nop 0
	v_add_u32_e32 v26, -1, v25
	v_fma_f32 v27, -v26, v25, v24
	v_cmp_ge_f32_e64 s[6:7], 0, v27
	v_add_u32_e32 v27, 1, v25
	s_nop 0
	v_cndmask_b32_e64 v26, v25, v26, s[6:7]
	v_fma_f32 v25, -v27, v25, v24
	v_cmp_lt_f32_e64 s[6:7], 0, v25
	s_nop 1
	v_cndmask_b32_e64 v25, v26, v27, s[6:7]
	v_mul_f32_e32 v26, 0x37800000, v25
	v_cndmask_b32_e32 v25, v25, v26, vcc
	v_cmp_class_f32_e32 vcc, v24, v194
	s_nop 1
	v_cndmask_b32_e32 v24, v25, v24, vcc
	v_div_scale_f32 v25, s[6:7], v24, v24, s70
	v_rcp_f32_e32 v26, v25
	s_nop 0
	v_fma_f32 v27, -v25, v26, 1.0
	v_fmac_f32_e32 v26, v27, v26
	v_div_scale_f32 v27, vcc, s70, v24, s70
	v_mul_f32_e32 v28, v27, v26
	v_fma_f32 v29, -v25, v28, v27
	v_fmac_f32_e32 v28, v29, v26
	v_fma_f32 v25, -v25, v28, v27
	v_div_fmas_f32 v25, v25, v26, v28
	v_div_fixup_f32 v24, v25, v24, s70
	v_pk_mul_f32 v[26:27], v[94:95], v[24:25] op_sel_hi:[1,0]
	v_pk_mul_f32 v[28:29], v[96:97], v[24:25] op_sel_hi:[1,0]
	s_nop 0
	v_pk_mul_f32 v[94:95], v[14:15], v[26:27]
	v_pk_mul_f32 v[26:27], v[90:91], v[24:25] op_sel_hi:[1,0]
	v_pk_mul_f32 v[96:97], v[16:17], v[28:29]
	v_pk_mul_f32 v[28:29], v[92:93], v[24:25] op_sel_hi:[1,0]
	v_pk_mul_f32 v[90:91], v[6:7], v[26:27]
	v_pk_mul_f32 v[26:27], v[86:87], v[24:25] op_sel_hi:[1,0]
	v_pk_mul_f32 v[92:93], v[8:9], v[28:29]
	v_pk_mul_f32 v[28:29], v[88:89], v[24:25] op_sel_hi:[1,0]
	v_pk_mul_f32 v[86:87], v[10:11], v[26:27]
	v_pk_mul_f32 v[26:27], v[82:83], v[24:25] op_sel_hi:[1,0]
	v_pk_mul_f32 v[24:25], v[84:85], v[24:25] op_sel_hi:[1,0]
	v_pk_mul_f32 v[88:89], v[12:13], v[28:29]
	v_pk_mul_f32 v[84:85], v[4:5], v[24:25]
	v_pk_mul_f32 v[82:83], v[2:3], v[26:27]
.LBB0_1067:
	s_mov_b64 s[6:7], 0x40000
	v_lshl_add_u64 v[28:29], v[22:23], 0, s[6:7]
	v_add_co_u32_e32 v22, vcc, 0x40000, v22
	v_cvt_pk_bf16_f32 v24, v94, v95
	v_cvt_pk_bf16_f32 v25, v96, v97
	v_cvt_pk_bf16_f32 v26, v90, v91
	v_cvt_pk_bf16_f32 v27, v92, v93
	s_nop 1
	v_addc_co_u32_e32 v23, vcc, 0, v23, vcc
	s_and_b64 vcc, exec, s[4:5]
	global_store_dwordx4 v[22:23], v[24:27], off
	v_cvt_pk_bf16_f32 v22, v86, v87
	v_cvt_pk_bf16_f32 v23, v88, v89
	s_nop 1
	v_cvt_pk_bf16_f32 v24, v82, v83
	v_cvt_pk_bf16_f32 v25, v84, v85
	global_store_dwordx4 v[28:29], v[22:25], off offset:64
	s_cbranch_vccnz .LBB0_1069
	s_nop 0
	v_pk_mul_f32 v[22:23], v[80:81], v[80:81]
	v_pk_mul_f32 v[24:25], v[78:79], v[78:79]
	s_nop 0
	v_pk_mov_b32 v[26:27], v[24:25], v[22:23] op_sel:[1,0]
	v_mov_b32_e32 v25, v23
	v_pk_add_f32 v[22:23], v[26:27], v[24:25]
	v_pk_mul_f32 v[24:25], v[76:77], v[76:77]
	v_pk_mul_f32 v[26:27], v[74:75], v[74:75]
	v_pk_add_f32 v[22:23], v[22:23], v[22:23] op_sel:[0,1] op_sel_hi:[1,0]
	v_pk_mov_b32 v[28:29], v[26:27], v[24:25] op_sel:[1,0]
	v_mov_b32_e32 v27, v25
	v_pk_add_f32 v[24:25], v[28:29], v[26:27]
	v_mul_f32_e32 v26, v66, v66
	v_mul_f32_e32 v27, v67, v67
	v_pk_add_f32 v[24:25], v[24:25], v[24:25] op_sel:[0,1] op_sel_hi:[1,0]
	v_mov_b32_e32 v23, v26
	v_mov_b32_e32 v25, v27
	v_pk_add_f32 v[22:23], v[22:23], v[24:25]
	v_mul_f32_e32 v24, v71, v71
	v_mul_f32_e32 v26, v73, v73
	v_mul_f32_e32 v28, v68, v68
	v_mul_f32_e32 v29, v69, v69
	v_pk_fma_f32 v[24:25], v[70:71], v[70:71], v[24:25] op_sel_hi:[1,1,0]
	v_pk_fma_f32 v[26:27], v[72:73], v[72:73], v[26:27] op_sel_hi:[1,1,0]
	v_mov_b32_e32 v25, v28
	v_mov_b32_e32 v27, v29
	v_pk_add_f32 v[24:25], v[24:25], v[26:27]
	s_nop 0
	v_pk_add_f32 v[22:23], v[22:23], v[24:25]
	v_and_b32_e32 v24, 64, v195
	v_add_f32_e32 v22, v22, v23
	v_xor_b32_e32 v23, 16, v195
	v_add_u32_e32 v24, 64, v24
	v_cmp_lt_i32_e32 vcc, v23, v24
	s_nop 1
	v_cndmask_b32_e32 v23, v195, v23, vcc
	v_lshlrev_b32_e32 v23, 2, v23
	ds_bpermute_b32 v23, v23, v22
	s_waitcnt lgkmcnt(0)
	v_add_f32_e32 v22, v22, v23
	v_xor_b32_e32 v23, 32, v195
	v_cmp_lt_i32_e32 vcc, v23, v24
	s_nop 1
	v_cndmask_b32_e32 v23, v195, v23, vcc
	v_lshlrev_b32_e32 v23, 2, v23
	ds_bpermute_b32 v23, v23, v22
	s_waitcnt lgkmcnt(0)
; template <bool F8OUT = false> __device__ __forceinline__ void head_tile_store(const f32x4 (&acc)[2][2][4][2], bf16_t* obase  , int opitch, const float* gain, float scale, const f32x2e* rope, int row0, int fq) {
;     ...
;             const int row = row0 + ai * HALF + m * 16;
;             f32x4 x[2][2];
; #pragma unroll
;             for (int bj = 0; bj < 2; ++bj)
; #pragma unroll
;                 for (int n = 0; n < 2; ++n) x[bj][n] = acc[ai][bj][m][n];
;             if (gain) {
;                 float ss = 0.f;
; #pragma unroll
;                 for (int bj = 0; bj < 2; ++bj)
; #pragma unroll
;                     for (int n = 0; n < 2; ++n) ss += (x[bj][n][0] * x[bj][n][0] + x[bj][n][1] * x[bj][n][1]) + (x[bj][n][2] * x[bj][n][2] + x[bj][n][3] * x[bj][n][3]);
;                 ss += __shfl_xor(ss, 16); ss += __shfl_xor(ss, 32);
;                 const float r = scale / sqrtf(ss * (1.f / 64.f) + 1e-6f);
; #pragma unroll
;                 for (int bj = 0; bj < 2; ++bj)
; #pragma unroll
;                     for (int n = 0; n < 2; ++n) x[bj][n] = x[bj][n] * r * g[bj][n];
;             }
;             if (rope) {
;                 const int t = row & 8191; const bool second = (fq & 2) != 0;
; #pragma unroll
;                 for (int bj = 0; bj < 2; ++bj) { const int pos = bj ? (t & 63) : (t >> 6); const f32x2e* tb = rope + pos * 16 + 8 * (fq & 1);
; #pragma unroll
;                     for (int n = 0; n < 2; ++n)
; #pragma unroll
;                         for (int e = 0; e < 4; ++e) { const float p = __shfl_xor(x[bj][n][e], 32); const f32x2e cs = tb[4 * n + e]; const float v = x[bj][n][e];
;                             x[bj][n][e] = second ? (p * cs.y + v * cs.x) : (v * cs.x - p * cs.y); } }
;             }
;             if constexpr (F8OUT) { unsigned char* rowp8 = (unsigned char*)obase + (size_t)row * opitch + 8 * fq; typedef unsigned u32x2_ __attribute__((ext_vector_type(2)));
; #pragma unroll
;                 for (int bj = 0; bj < 2; ++bj) *(u32x2_*)(rowp8 + 32 * bj) = (u32x2_){pk4_fp8(x[bj][0][0], x[bj][0][1], x[bj][0][2], x[bj][0][3]), pk4_fp8(x[bj][1][0], x[bj][1][1], x[bj][1][2], x[bj][1][3])};
;                 continue; }
;             bf16_t* rowp = obase + (size_t)row * opitch + 8 * fq;
; #pragma unroll
	v_add_f32_e32 v22, v22, v23
	v_fmamk_f32 v22, v22, 0x3c800000, v193
	v_mul_f32_e32 v23, 0x4f800000, v22
	v_cmp_gt_f32_e32 vcc, s69, v22
	s_nop 1
	v_cndmask_b32_e32 v22, v22, v23, vcc
	v_sqrt_f32_e32 v23, v22
	s_nop 0
	v_add_u32_e32 v24, -1, v23
	v_fma_f32 v25, -v24, v23, v22
	v_cmp_ge_f32_e64 s[6:7], 0, v25
	v_add_u32_e32 v25, 1, v23
	s_nop 0
	v_cndmask_b32_e64 v24, v23, v24, s[6:7]
	v_fma_f32 v23, -v25, v23, v22
	v_cmp_lt_f32_e64 s[6:7], 0, v23
	s_nop 1
	v_cndmask_b32_e64 v23, v24, v25, s[6:7]
	v_mul_f32_e32 v24, 0x37800000, v23
	v_cndmask_b32_e32 v23, v23, v24, vcc
	v_cmp_class_f32_e32 vcc, v22, v194
	s_nop 1
	v_cndmask_b32_e32 v22, v23, v22, vcc
	v_div_scale_f32 v23, s[6:7], v22, v22, s70
	v_rcp_f32_e32 v24, v23
	s_nop 0
	v_fma_f32 v25, -v23, v24, 1.0
	v_fmac_f32_e32 v24, v25, v24
	v_div_scale_f32 v25, vcc, s70, v22, s70
	v_mul_f32_e32 v26, v25, v24
	v_fma_f32 v27, -v23, v26, v25
	v_fmac_f32_e32 v26, v27, v24
	v_fma_f32 v23, -v23, v26, v25
	v_div_fmas_f32 v23, v23, v24, v26
	v_div_fixup_f32 v22, v23, v22, s70
	v_pk_mul_f32 v[24:25], v[78:79], v[22:23] op_sel_hi:[1,0]
	v_pk_mul_f32 v[26:27], v[80:81], v[22:23] op_sel_hi:[1,0]
	s_nop 0
	v_pk_mul_f32 v[78:79], v[14:15], v[24:25]
	v_pk_mul_f32 v[24:25], v[74:75], v[22:23] op_sel_hi:[1,0]
	v_pk_mul_f32 v[80:81], v[16:17], v[26:27]
	v_pk_mul_f32 v[26:27], v[76:77], v[22:23] op_sel_hi:[1,0]
	v_pk_mul_f32 v[74:75], v[6:7], v[24:25]
	v_pk_mul_f32 v[24:25], v[70:71], v[22:23] op_sel_hi:[1,0]
	v_pk_mul_f32 v[76:77], v[8:9], v[26:27]
	v_pk_mul_f32 v[26:27], v[72:73], v[22:23] op_sel_hi:[1,0]
	v_pk_mul_f32 v[70:71], v[10:11], v[24:25]
	v_pk_mul_f32 v[24:25], v[66:67], v[22:23] op_sel_hi:[1,0]
	v_pk_mul_f32 v[22:23], v[68:69], v[22:23] op_sel_hi:[1,0]
	v_pk_mul_f32 v[72:73], v[12:13], v[26:27]
	v_pk_mul_f32 v[68:69], v[4:5], v[22:23]
	v_pk_mul_f32 v[66:67], v[2:3], v[24:25]
.LBB0_1069:
	s_nop 0
	v_lshlrev_b64 v[22:23], 11, v[18:19]
	v_lshl_add_u64 v[22:23], v[20:21], 0, v[22:23]
	v_add_co_u32_e32 v30, vcc, 0x48000, v22
	s_mov_b64 s[6:7], 0x48000
	s_nop 0
	v_addc_co_u32_e32 v31, vcc, 0, v23, vcc
	v_lshl_add_u64 v[28:29], v[22:23], 0, s[6:7]
	v_cvt_pk_bf16_f32 v24, v78, v79
	v_cvt_pk_bf16_f32 v25, v80, v81
	v_cvt_pk_bf16_f32 v26, v74, v75
	v_cvt_pk_bf16_f32 v27, v76, v77
	s_and_b64 vcc, exec, s[4:5]
	global_store_dwordx4 v[30:31], v[24:27], off
	s_nop 1
	v_cvt_pk_bf16_f32 v24, v70, v71
	v_cvt_pk_bf16_f32 v25, v72, v73
	v_cvt_pk_bf16_f32 v26, v66, v67
	v_cvt_pk_bf16_f32 v27, v68, v69
	global_store_dwordx4 v[28:29], v[24:27], off offset:64
	s_cbranch_vccnz .LBB0_1071
	s_nop 0
	v_pk_mul_f32 v[24:25], v[64:65], v[64:65]
	v_pk_mul_f32 v[26:27], v[62:63], v[62:63]
	s_nop 0
	v_pk_mov_b32 v[28:29], v[26:27], v[24:25] op_sel:[1,0]
	v_mov_b32_e32 v27, v25
	v_pk_add_f32 v[24:25], v[28:29], v[26:27]
	v_pk_mul_f32 v[26:27], v[60:61], v[60:61]
	v_pk_mul_f32 v[28:29], v[58:59], v[58:59]
	v_pk_add_f32 v[24:25], v[24:25], v[24:25] op_sel:[0,1] op_sel_hi:[1,0]
	v_pk_mov_b32 v[30:31], v[28:29], v[26:27] op_sel:[1,0]
	v_mov_b32_e32 v29, v27
	v_pk_add_f32 v[26:27], v[30:31], v[28:29]
	v_mul_f32_e32 v28, v50, v50
	v_mul_f32_e32 v29, v51, v51
	v_pk_add_f32 v[26:27], v[26:27], v[26:27] op_sel:[0,1] op_sel_hi:[1,0]
	v_mov_b32_e32 v25, v28
	v_mov_b32_e32 v27, v29
	v_pk_add_f32 v[24:25], v[24:25], v[26:27]
	v_mul_f32_e32 v26, v55, v55
	v_mul_f32_e32 v28, v57, v57
	v_mul_f32_e32 v30, v52, v52
	v_mul_f32_e32 v31, v53, v53
	v_pk_fma_f32 v[26:27], v[54:55], v[54:55], v[26:27] op_sel_hi:[1,1,0]
	v_pk_fma_f32 v[28:29], v[56:57], v[56:57], v[28:29] op_sel_hi:[1,1,0]
	v_mov_b32_e32 v27, v30
	v_mov_b32_e32 v29, v31
	v_pk_add_f32 v[26:27], v[26:27], v[28:29]
	s_nop 0
	v_pk_add_f32 v[24:25], v[24:25], v[26:27]
	v_and_b32_e32 v26, 64, v195
	v_add_f32_e32 v24, v24, v25
	v_xor_b32_e32 v25, 16, v195
	v_add_u32_e32 v26, 64, v26
	v_cmp_lt_i32_e32 vcc, v25, v26
	s_nop 1
	v_cndmask_b32_e32 v25, v195, v25, vcc
	v_lshlrev_b32_e32 v25, 2, v25
	ds_bpermute_b32 v25, v25, v24
	s_waitcnt lgkmcnt(0)
	v_add_f32_e32 v24, v24, v25
	v_xor_b32_e32 v25, 32, v195
	v_cmp_lt_i32_e32 vcc, v25, v26
	s_nop 1
	v_cndmask_b32_e32 v25, v195, v25, vcc
	v_lshlrev_b32_e32 v25, 2, v25
	ds_bpermute_b32 v25, v25, v24
	s_waitcnt lgkmcnt(0)
	v_add_f32_e32 v24, v24, v25
	v_fmamk_f32 v24, v24, 0x3c800000, v193
	v_mul_f32_e32 v25, 0x4f800000, v24
	v_cmp_gt_f32_e32 vcc, s69, v24
	s_nop 1
	v_cndmask_b32_e32 v24, v24, v25, vcc
	v_sqrt_f32_e32 v25, v24
	s_nop 0
	v_add_u32_e32 v26, -1, v25
	v_fma_f32 v27, -v26, v25, v24
	v_cmp_ge_f32_e64 s[6:7], 0, v27
	v_add_u32_e32 v27, 1, v25
	s_nop 0
	v_cndmask_b32_e64 v26, v25, v26, s[6:7]
	v_fma_f32 v25, -v27, v25, v24
	v_cmp_lt_f32_e64 s[6:7], 0, v25
	s_nop 1
	v_cndmask_b32_e64 v25, v26, v27, s[6:7]
	v_mul_f32_e32 v26, 0x37800000, v25
	v_cndmask_b32_e32 v25, v25, v26, vcc
	v_cmp_class_f32_e32 vcc, v24, v194
	s_nop 1
	v_cndmask_b32_e32 v24, v25, v24, vcc
	v_div_scale_f32 v25, s[6:7], v24, v24, s70
	v_rcp_f32_e32 v26, v25
	s_nop 0
	v_fma_f32 v27, -v25, v26, 1.0
	v_fmac_f32_e32 v26, v27, v26
	v_div_scale_f32 v27, vcc, s70, v24, s70
	v_mul_f32_e32 v28, v27, v26
	v_fma_f32 v29, -v25, v28, v27
	v_fmac_f32_e32 v28, v29, v26
	v_fma_f32 v25, -v25, v28, v27
	v_div_fmas_f32 v25, v25, v26, v28
	v_div_fixup_f32 v24, v25, v24, s70
	v_pk_mul_f32 v[26:27], v[62:63], v[24:25] op_sel_hi:[1,0]
	v_pk_mul_f32 v[28:29], v[64:65], v[24:25] op_sel_hi:[1,0]
	s_nop 0
	v_pk_mul_f32 v[62:63], v[14:15], v[26:27]
	v_pk_mul_f32 v[26:27], v[58:59], v[24:25] op_sel_hi:[1,0]
	v_pk_mul_f32 v[64:65], v[16:17], v[28:29]
	v_pk_mul_f32 v[28:29], v[60:61], v[24:25] op_sel_hi:[1,0]
	v_pk_mul_f32 v[58:59], v[6:7], v[26:27]
	v_pk_mul_f32 v[26:27], v[54:55], v[24:25] op_sel_hi:[1,0]
	v_pk_mul_f32 v[60:61], v[8:9], v[28:29]
	v_pk_mul_f32 v[28:29], v[56:57], v[24:25] op_sel_hi:[1,0]
	v_pk_mul_f32 v[54:55], v[10:11], v[26:27]
	v_pk_mul_f32 v[26:27], v[50:51], v[24:25] op_sel_hi:[1,0]
	v_pk_mul_f32 v[24:25], v[52:53], v[24:25] op_sel_hi:[1,0]
	v_pk_mul_f32 v[56:57], v[12:13], v[28:29]
	v_pk_mul_f32 v[52:53], v[4:5], v[24:25]
	v_pk_mul_f32 v[50:51], v[2:3], v[26:27]
; __device__ __forceinline__ unsigned cvt_pk_bf16(float lo, float hi) { unsigned r; asm volatile("v_cvt_pk_bf16_f32 %0, %1, %2" : "=v"(r) : "v"(lo), "v"(hi)); return r; }
; template <bool F8OUT = false> __device__ __forceinline__ void head_tile_store(const f32x4 (&acc)[2][2][4][2], bf16_t* obase  , int opitch, const float* gain, float scale, const f32x2e* rope, int row0, int fq) {
;     ...
;             if (gain) {
;                 float ss = 0.f;
; #pragma unroll
;                 for (int bj = 0; bj < 2; ++bj)
; #pragma unroll
;                     for (int n = 0; n < 2; ++n) ss += (x[bj][n][0] * x[bj][n][0] + x[bj][n][1] * x[bj][n][1]) + (x[bj][n][2] * x[bj][n][2] + x[bj][n][3] * x[bj][n][3]);
;                 ss += __shfl_xor(ss, 16); ss += __shfl_xor(ss, 32);
;                 const float r = scale / sqrtf(ss * (1.f / 64.f) + 1e-6f);
; #pragma unroll
;                 for (int bj = 0; bj < 2; ++bj)
; #pragma unroll
;                     for (int n = 0; n < 2; ++n) x[bj][n] = x[bj][n] * r * g[bj][n];
;             }
;     ...
;             bf16_t* rowp = obase + (size_t)row * opitch + 8 * fq;
; #pragma unroll
;             for (int bj = 0; bj < 2; ++bj) { u32x4 w; w.x = cvt_pk_bf16(x[bj][0][0], x[bj][0][1]); w.y = cvt_pk_bf16(x[bj][0][2], x[bj][0][3]); w.z = cvt_pk_bf16(x[bj][1][0], x[bj][1][1]); w.w = cvt_pk_bf16(x[bj][1][2], x[bj][1][3]);
;                 *(u32x4*)(rowp + 32 * bj) = w; }
.LBB0_1071:
	s_mov_b64 s[6:7], 0x50000
	v_lshl_add_u64 v[28:29], v[22:23], 0, s[6:7]
	v_add_co_u32_e32 v22, vcc, 0x50000, v22
	v_cvt_pk_bf16_f32 v24, v62, v63
	v_cvt_pk_bf16_f32 v25, v64, v65
	v_cvt_pk_bf16_f32 v26, v58, v59
	v_cvt_pk_bf16_f32 v27, v60, v61
	s_nop 1
	v_addc_co_u32_e32 v23, vcc, 0, v23, vcc
	s_and_b64 vcc, exec, s[4:5]
	global_store_dwordx4 v[22:23], v[24:27], off
	v_cvt_pk_bf16_f32 v22, v54, v55
	v_cvt_pk_bf16_f32 v23, v56, v57
	s_nop 1
	v_cvt_pk_bf16_f32 v24, v50, v51
	v_cvt_pk_bf16_f32 v25, v52, v53
	global_store_dwordx4 v[28:29], v[22:25], off offset:64
	s_cbranch_vccnz .LBB0_1073
	s_nop 0
	v_pk_mul_f32 v[22:23], v[48:49], v[48:49]
	v_pk_mul_f32 v[24:25], v[46:47], v[46:47]
	s_nop 0
	v_pk_mov_b32 v[26:27], v[24:25], v[22:23] op_sel:[1,0]
	v_mov_b32_e32 v25, v23
	v_pk_add_f32 v[22:23], v[26:27], v[24:25]
	v_pk_mul_f32 v[24:25], v[44:45], v[44:45]
	v_pk_mul_f32 v[26:27], v[42:43], v[42:43]
	v_pk_add_f32 v[22:23], v[22:23], v[22:23] op_sel:[0,1] op_sel_hi:[1,0]
	v_pk_mov_b32 v[28:29], v[26:27], v[24:25] op_sel:[1,0]
	v_mov_b32_e32 v27, v25
	v_pk_add_f32 v[24:25], v[28:29], v[26:27]
	v_mul_f32_e32 v26, v34, v34
	v_mul_f32_e32 v27, v35, v35
	v_pk_add_f32 v[24:25], v[24:25], v[24:25] op_sel:[0,1] op_sel_hi:[1,0]
	v_mov_b32_e32 v23, v26
	v_mov_b32_e32 v25, v27
	v_pk_add_f32 v[22:23], v[22:23], v[24:25]
	v_mul_f32_e32 v24, v39, v39
	v_mul_f32_e32 v26, v41, v41
	v_mul_f32_e32 v28, v36, v36
	v_mul_f32_e32 v29, v37, v37
	v_pk_fma_f32 v[24:25], v[38:39], v[38:39], v[24:25] op_sel_hi:[1,1,0]
	v_pk_fma_f32 v[26:27], v[40:41], v[40:41], v[26:27] op_sel_hi:[1,1,0]
	v_mov_b32_e32 v25, v28
	v_mov_b32_e32 v27, v29
	v_pk_add_f32 v[24:25], v[24:25], v[26:27]
	s_nop 0
	v_pk_add_f32 v[22:23], v[22:23], v[24:25]
	v_and_b32_e32 v24, 64, v195
	v_add_f32_e32 v22, v22, v23
	v_xor_b32_e32 v23, 16, v195
	v_add_u32_e32 v24, 64, v24
	v_cmp_lt_i32_e32 vcc, v23, v24
	s_nop 1
	v_cndmask_b32_e32 v23, v195, v23, vcc
	v_lshlrev_b32_e32 v23, 2, v23
	ds_bpermute_b32 v23, v23, v22
	s_waitcnt lgkmcnt(0)
	v_add_f32_e32 v22, v22, v23
	v_xor_b32_e32 v23, 32, v195
	v_cmp_lt_i32_e32 vcc, v23, v24
	s_nop 1
	v_cndmask_b32_e32 v23, v195, v23, vcc
	v_lshlrev_b32_e32 v23, 2, v23
	ds_bpermute_b32 v23, v23, v22
	s_waitcnt lgkmcnt(0)
	v_add_f32_e32 v22, v22, v23
	v_fmamk_f32 v22, v22, 0x3c800000, v193
	v_mul_f32_e32 v23, 0x4f800000, v22
	v_cmp_gt_f32_e32 vcc, s69, v22
	s_nop 1
	v_cndmask_b32_e32 v22, v22, v23, vcc
	v_sqrt_f32_e32 v23, v22
	s_nop 0
	v_add_u32_e32 v24, -1, v23
	v_fma_f32 v25, -v24, v23, v22
	v_cmp_ge_f32_e64 s[4:5], 0, v25
	v_add_u32_e32 v25, 1, v23
	s_nop 0
	v_cndmask_b32_e64 v24, v23, v24, s[4:5]
	v_fma_f32 v23, -v25, v23, v22
	v_cmp_lt_f32_e64 s[4:5], 0, v23
	s_nop 1
	v_cndmask_b32_e64 v23, v24, v25, s[4:5]
	v_mul_f32_e32 v24, 0x37800000, v23
	v_cndmask_b32_e32 v23, v23, v24, vcc
	v_cmp_class_f32_e32 vcc, v22, v194
	s_nop 1
	v_cndmask_b32_e32 v22, v23, v22, vcc
	v_div_scale_f32 v23, s[4:5], v22, v22, s70
	v_rcp_f32_e32 v24, v23
	s_nop 0
	v_fma_f32 v25, -v23, v24, 1.0
	v_fmac_f32_e32 v24, v25, v24
	v_div_scale_f32 v25, vcc, s70, v22, s70
	v_mul_f32_e32 v26, v25, v24
	v_fma_f32 v27, -v23, v26, v25
	v_fmac_f32_e32 v26, v27, v24
	v_fma_f32 v23, -v23, v26, v25
	v_div_fmas_f32 v23, v23, v24, v26
	v_div_fixup_f32 v22, v23, v22, s70
	v_pk_mul_f32 v[24:25], v[46:47], v[22:23] op_sel_hi:[1,0]
	v_pk_mul_f32 v[26:27], v[48:49], v[22:23] op_sel_hi:[1,0]
	s_nop 0
	v_pk_mul_f32 v[46:47], v[14:15], v[24:25]
	v_pk_mul_f32 v[48:49], v[16:17], v[26:27]
	v_pk_mul_f32 v[14:15], v[42:43], v[22:23] op_sel_hi:[1,0]
	v_pk_mul_f32 v[16:17], v[44:45], v[22:23] op_sel_hi:[1,0]
	v_pk_mul_f32 v[42:43], v[6:7], v[14:15]
	v_pk_mul_f32 v[44:45], v[8:9], v[16:17]
	v_pk_mul_f32 v[6:7], v[38:39], v[22:23] op_sel_hi:[1,0]
	v_pk_mul_f32 v[8:9], v[40:41], v[22:23] op_sel_hi:[1,0]
	v_pk_mul_f32 v[38:39], v[10:11], v[6:7]
	v_pk_mul_f32 v[40:41], v[12:13], v[8:9]
	v_pk_mul_f32 v[6:7], v[34:35], v[22:23] op_sel_hi:[1,0]
	v_pk_mul_f32 v[8:9], v[36:37], v[22:23] op_sel_hi:[1,0]
	v_pk_mul_f32 v[34:35], v[2:3], v[6:7]
	v_pk_mul_f32 v[36:37], v[4:5], v[8:9]
.LBB0_1073:
	s_nop 0
	v_lshlrev_b64 v[2:3], 11, v[18:19]
	v_lshl_add_u64 v[8:9], v[20:21], 0, v[2:3]
	s_mov_b64 s[4:5], 0x58000
	v_lshl_add_u64 v[6:7], v[8:9], 0, s[4:5]
	s_mov_b32 s4, 0x58000
	v_add_co_u32_e32 v8, vcc, s4, v8
	v_cvt_pk_bf16_f32 v2, v46, v47
	v_cvt_pk_bf16_f32 v3, v48, v49
	v_cvt_pk_bf16_f32 v4, v42, v43
	v_cvt_pk_bf16_f32 v5, v44, v45
	s_nop 1
	v_addc_co_u32_e32 v9, vcc, 0, v9, vcc
	global_store_dwordx4 v[8:9], v[2:5], off
	s_nop 1
	v_cvt_pk_bf16_f32 v2, v38, v39
	v_cvt_pk_bf16_f32 v3, v40, v41
	v_cvt_pk_bf16_f32 v4, v34, v35
	v_cvt_pk_bf16_f32 v5, v36, v37
	s_andn2_b64 vcc, exec, s[2:3]
	s_mov_b64 s[2:3], -1
	global_store_dwordx4 v[6:7], v[2:5], off offset:64
	s_cbranch_vccnz .LBB0_1022
